# MoE K-loops (phases 8/9): waves 4-7 do the weight-tile convert/LDS-write block before the fragment reads + MFMAs (waves 0-3 keep original order) so MFMA bursts of SIMD-sharing waves interleave
# speedup vs baseline: 1.0128x; 1.0005x over previous
.LBB0_1013:
	s_or_b64 exec, exec, s[34:35]
	s_lshl_b64 s[34:35], s[10:11], 22
	s_add_u32 s10, s12, s34
	s_addc_u32 s52, s13, s35
	s_lshl_b32 s34, s36, 9
	s_lshl_b32 s35, s46, 6
	s_sub_i32 s34, s35, s34
	s_ashr_i32 s35, s34, 31
	s_lshl_b64 s[36:37], s[34:35], 2
	s_add_u32 s36, s10, s36
	s_addc_u32 s37, s52, s37
	v_or_b32_e32 v146, v3, v1
	s_waitcnt lgkmcnt(0)
	v_readfirstlane_b32 s51, v2
	v_lshl_add_u64 v[2:3], s[36:37], 0, v[152:153]
	v_lshl_add_u64 v[156:157], v[2:3], 0, v[148:149]
	s_mov_b64 s[36:37], -1
	s_cmp_ge_i32 s38, s50
	v_lshl_add_u64 v[132:133], v[156:157], 0, s[22:23]
	v_lshl_add_u64 v[130:131], v[156:157], 0, s[24:25]
	v_lshl_add_u64 v[134:135], v[156:157], 0, s[26:27]
	v_lshl_add_u64 v[138:139], v[156:157], 0, s[28:29]
	v_lshl_add_u64 v[142:143], v[156:157], 0, s[30:31]
	s_cbranch_scc0 .LBB0_1017
	global_load_dwordx4 v[2:5], v[156:157], off sc1 nt
	s_mov_b32 m0, s39
	global_load_dwordx4 v[6:9], v[132:133], off sc1 nt
	v_lshl_add_u64 v[50:51], s[14:15], 0, v[146:147]
	global_load_lds_dwordx4 v146, s[14:15]
	global_load_dwordx4 v[34:37], v[130:131], off sc1 nt
	global_load_dwordx4 v[38:41], v[134:135], off sc1 nt
	s_mov_b32 m0, s40
	s_nop 0
	global_load_lds_dwordx4 v146, s[16:17]
	s_waitcnt vmcnt(4)
	s_nop 0
	v_cvt_pk_bf16_f32 v2, v2, v6
	ds_write_b32 v169, v2 offset:49152
	v_cvt_pk_bf16_f32 v2, v3, v7
	ds_write_b32 v169, v2 offset:49216
	v_cvt_pk_bf16_f32 v2, v4, v8
	ds_write_b32 v169, v2 offset:49280
	v_cvt_pk_bf16_f32 v2, v5, v9
	ds_write_b32 v169, v2 offset:49344
	global_load_dwordx4 v[42:45], v[138:139], off sc1 nt
	global_load_dwordx4 v[46:49], v[142:143], off sc1 nt
	s_waitcnt vmcnt(5)
	s_mov_b32 m0, s41
	s_waitcnt lgkmcnt(0)
	s_barrier
	global_load_lds_dwordx4 v146, s[18:19]
	v_mov_b32_e32 v2, 0
	s_mov_b32 s37, -2
	s_movk_i32 s36, 0x80
	v_mov_b32_e32 v3, v2
	v_mov_b32_e32 v4, v2
	v_mov_b32_e32 v5, v2
	v_mov_b32_e32 v6, v2
	v_mov_b32_e32 v7, v2
	v_mov_b32_e32 v8, v2
	v_mov_b32_e32 v9, v2
	v_mov_b32_e32 v10, v2
	v_mov_b32_e32 v11, v2
	v_mov_b32_e32 v12, v2
	v_mov_b32_e32 v13, v2
	v_mov_b32_e32 v14, v2
	v_mov_b32_e32 v15, v2
	v_mov_b32_e32 v16, v2
	v_mov_b32_e32 v17, v2
	v_mov_b32_e32 v66, v2
	v_mov_b32_e32 v67, v2
	v_mov_b32_e32 v68, v2
	v_mov_b32_e32 v69, v2
	v_mov_b32_e32 v70, v2
	v_mov_b32_e32 v71, v2
	v_mov_b32_e32 v72, v2
	v_mov_b32_e32 v73, v2
	v_mov_b32_e32 v74, v2
	v_mov_b32_e32 v75, v2
	v_mov_b32_e32 v76, v2
	v_mov_b32_e32 v77, v2
	v_mov_b32_e32 v78, v2
	v_mov_b32_e32 v79, v2
	v_mov_b32_e32 v80, v2
	v_mov_b32_e32 v81, v2
	v_mov_b32_e32 v18, v2
	v_mov_b32_e32 v19, v2
	v_mov_b32_e32 v20, v2
	v_mov_b32_e32 v21, v2
	v_mov_b32_e32 v22, v2
	v_mov_b32_e32 v23, v2
	v_mov_b32_e32 v24, v2
	v_mov_b32_e32 v25, v2
	v_mov_b32_e32 v26, v2
	v_mov_b32_e32 v27, v2
	v_mov_b32_e32 v28, v2
	v_mov_b32_e32 v29, v2
	v_mov_b32_e32 v30, v2
	v_mov_b32_e32 v31, v2
	v_mov_b32_e32 v32, v2
	v_mov_b32_e32 v33, v2
	v_mov_b32_e32 v114, v2
	v_mov_b32_e32 v115, v2
	v_mov_b32_e32 v116, v2
	v_mov_b32_e32 v117, v2
	v_mov_b32_e32 v118, v2
	v_mov_b32_e32 v119, v2
	v_mov_b32_e32 v120, v2
	v_mov_b32_e32 v121, v2
	v_mov_b32_e32 v122, v2
	v_mov_b32_e32 v123, v2
	v_mov_b32_e32 v124, v2
	v_mov_b32_e32 v125, v2
	v_mov_b32_e32 v126, v2
	v_mov_b32_e32 v127, v2
	v_mov_b32_e32 v128, v2
	v_mov_b32_e32 v129, v2
	v_readfirstlane_b32 s98, v250
	s_bitcmp1_b32 s98, 8
	s_cbranch_scc1 .Lmoe_B_1015
.LBB0_1015:
	s_mul_i32 s53, s37, 0xab
	s_add_i32 s10, s53, 0x357
	s_bfe_u32 s10, s10, 0x70009
	s_mul_i32 s10, s10, 3
	s_sub_i32 s10, s37, s10
	s_add_i32 s10, s10, 5
	s_and_b32 s10, s10, 0xff
	s_lshl_b32 s10, s10, 14
	s_add_i32 s56, s39, s10
	s_add_i32 s52, s37, 2
	v_add_u32_e32 v93, s56, v160
	v_add_u32_e32 v52, v93, v163
	v_add_u32_e32 v92, v161, v162
	ds_read_b64 v[64:65], v52
	ds_read_b128 v[52:55], v92 offset:49152
	ds_read_b128 v[56:59], v92 offset:51200
	ds_read_b128 v[60:63], v92 offset:53248
	ds_read_b128 v[82:85], v92 offset:55296
	s_waitcnt lgkmcnt(0)
	v_cvt_pk_f32_fp8_e32 v[86:87], v64
	v_cvt_pk_f32_fp8_sdwa v[88:89], v64 src0_sel:WORD_1
	v_cvt_pk_f32_fp8_e32 v[90:91], v65
	v_cvt_pk_f32_fp8_sdwa v[64:65], v65 src0_sel:WORD_1
	v_cvt_pk_bf16_f32 v86, v86, v87
	v_cvt_pk_bf16_f32 v87, v88, v89
	v_cvt_pk_bf16_f32 v88, v90, v91
	v_cvt_pk_bf16_f32 v89, v64, v65
	s_waitcnt vmcnt(4)
	s_sub_i32 s10, s36, 32
	v_cvt_pk_bf16_f32 v34, v34, v38
	s_cmp_lt_u32 s52, 61
	ds_write_b32 v169, v34 offset:57344
	v_cvt_pk_bf16_f32 v34, v35, v39
	s_cselect_b32 s10, s10, 0x7e0
	ds_write_b32 v169, v34 offset:57408
	v_cvt_pk_bf16_f32 v34, v36, v40
	s_lshl_b64 s[54:55], s[10:11], 11
	ds_write_b32 v169, v34 offset:57472
	v_cvt_pk_bf16_f32 v34, v37, v41
	ds_write_b32 v169, v34 offset:57536
	v_lshl_add_u64 v[38:39], v[156:157], 0, s[54:55]
	global_load_dwordx4 v[34:37], v[38:39], off sc1 nt
	v_lshl_add_u64 v[38:39], v[38:39], 0, s[22:23]
	global_load_dwordx4 v[38:41], v[38:39], off sc1 nt
	v_mfma_f32_32x32x16_bf16 v[114:129], v[52:55], v[86:89], v[114:129]
	v_mfma_f32_32x32x16_bf16 v[18:33], v[56:59], v[86:89], v[18:33]
	v_mfma_f32_32x32x16_bf16 v[66:81], v[60:63], v[86:89], v[66:81]
	v_mfma_f32_32x32x16_bf16 v[2:17], v[82:85], v[86:89], v[2:17]
	v_add_u32_e32 v52, v93, v165
	v_add_u32_e32 v94, v161, v164
	ds_read_b64 v[64:65], v52
	ds_read_b128 v[52:55], v94 offset:49152
	ds_read_b128 v[56:59], v94 offset:51200
	ds_read_b128 v[60:63], v94 offset:53248
	ds_read_b128 v[82:85], v94 offset:55296
	s_waitcnt lgkmcnt(0)
	v_cvt_pk_f32_fp8_e32 v[86:87], v64
	v_cvt_pk_f32_fp8_sdwa v[88:89], v64 src0_sel:WORD_1
	v_cvt_pk_f32_fp8_e32 v[90:91], v65
	v_cvt_pk_f32_fp8_sdwa v[64:65], v65 src0_sel:WORD_1
	v_cvt_pk_bf16_f32 v86, v86, v87
	v_cvt_pk_bf16_f32 v87, v88, v89
	v_cvt_pk_bf16_f32 v88, v90, v91
	v_cvt_pk_bf16_f32 v89, v64, v65
	s_nop 0
	v_mfma_f32_32x32x16_bf16 v[114:129], v[52:55], v[86:89], v[114:129]
	v_mfma_f32_32x32x16_bf16 v[18:33], v[56:59], v[86:89], v[18:33]
	v_mfma_f32_32x32x16_bf16 v[66:81], v[60:63], v[86:89], v[66:81]
	v_mfma_f32_32x32x16_bf16 v[2:17], v[82:85], v[86:89], v[2:17]
	s_waitcnt vmcnt(5)
	s_mov_b32 m0, s56
	s_waitcnt lgkmcnt(0)
	s_barrier
	v_lshl_add_u64 v[52:53], v[50:51], 0, s[10:11]
	global_load_lds_dwordx4 v[52:53], off
	s_addk_i32 s53, 0x402
	s_bfe_u32 s10, s53, 0x70009
	s_mul_i32 s10, s10, 3
	s_sub_i32 s10, s37, s10
	s_add_i32 s10, s10, 6
	s_and_b32 s10, s10, 0xff
	s_lshl_b32 s10, s10, 14
	s_add_i32 s37, s39, s10
	v_add_u32_e32 v93, s37, v160
	v_add_u32_e32 v52, v93, v163
	ds_read_b64 v[64:65], v52
	ds_read_b128 v[52:55], v92 offset:57344
	ds_read_b128 v[56:59], v92 offset:59392
	ds_read_b128 v[60:63], v92 offset:61440
	ds_read_b128 v[82:85], v92 offset:63488
	s_waitcnt lgkmcnt(0)
	v_cvt_pk_f32_fp8_e32 v[86:87], v64
	v_cvt_pk_f32_fp8_sdwa v[88:89], v64 src0_sel:WORD_1
	v_cvt_pk_f32_fp8_e32 v[90:91], v65
	v_cvt_pk_f32_fp8_sdwa v[64:65], v65 src0_sel:WORD_1
	v_cvt_pk_bf16_f32 v86, v86, v87
	v_cvt_pk_bf16_f32 v87, v88, v89
	v_cvt_pk_bf16_f32 v88, v90, v91
	v_cvt_pk_bf16_f32 v89, v64, v65
	s_waitcnt vmcnt(4)
	s_cmp_lt_u32 s52, 60
	v_cvt_pk_bf16_f32 v42, v42, v46
	ds_write_b32 v169, v42 offset:49152
	v_cvt_pk_bf16_f32 v42, v43, v47
	s_cselect_b32 s10, s36, 0x7e0
	ds_write_b32 v169, v42 offset:49216
	v_cvt_pk_bf16_f32 v42, v44, v48
	s_lshl_b64 s[54:55], s[10:11], 11
	ds_write_b32 v169, v42 offset:49280
	v_cvt_pk_bf16_f32 v42, v45, v49
	ds_write_b32 v169, v42 offset:49344
	v_lshl_add_u64 v[46:47], v[156:157], 0, s[54:55]
	global_load_dwordx4 v[42:45], v[46:47], off sc1 nt
	v_lshl_add_u64 v[46:47], v[46:47], 0, s[22:23]
	global_load_dwordx4 v[46:49], v[46:47], off sc1 nt
	v_mfma_f32_32x32x16_bf16 v[114:129], v[52:55], v[86:89], v[114:129]
	v_mfma_f32_32x32x16_bf16 v[18:33], v[56:59], v[86:89], v[18:33]
	v_mfma_f32_32x32x16_bf16 v[66:81], v[60:63], v[86:89], v[66:81]
	v_mfma_f32_32x32x16_bf16 v[2:17], v[82:85], v[86:89], v[2:17]
	v_add_u32_e32 v52, v93, v165
	ds_read_b64 v[64:65], v52
	ds_read_b128 v[52:55], v94 offset:57344
	ds_read_b128 v[56:59], v94 offset:59392
	ds_read_b128 v[60:63], v94 offset:61440
	ds_read_b128 v[82:85], v94 offset:63488
	s_waitcnt lgkmcnt(0)
	v_cvt_pk_f32_fp8_e32 v[86:87], v64
	v_cvt_pk_f32_fp8_sdwa v[88:89], v64 src0_sel:WORD_1
	v_cvt_pk_f32_fp8_e32 v[90:91], v65
	v_cvt_pk_f32_fp8_sdwa v[64:65], v65 src0_sel:WORD_1
	v_cvt_pk_bf16_f32 v86, v86, v87
	v_cvt_pk_bf16_f32 v87, v88, v89
	v_cvt_pk_bf16_f32 v88, v90, v91
	v_cvt_pk_bf16_f32 v89, v64, v65
	s_nop 0
	v_mfma_f32_32x32x16_bf16 v[114:129], v[52:55], v[86:89], v[114:129]
	v_mfma_f32_32x32x16_bf16 v[18:33], v[56:59], v[86:89], v[18:33]
	v_mfma_f32_32x32x16_bf16 v[66:81], v[60:63], v[86:89], v[66:81]
	v_mfma_f32_32x32x16_bf16 v[2:17], v[82:85], v[86:89], v[2:17]
	s_waitcnt vmcnt(5)
	s_mov_b32 m0, s37
	s_waitcnt lgkmcnt(0)
	s_barrier
	v_lshl_add_u64 v[52:53], v[50:51], 0, s[10:11]
	global_load_lds_dwordx4 v[52:53], off
	s_add_i32 s36, s36, 64
	s_cmp_gt_u32 s52, 61
	s_mov_b32 s37, s52
	s_cbranch_scc0 .LBB0_1015
	s_branch .Lmoe_X_1015
.Lmoe_B_1015:
	s_mul_i32 s53, s37, 0xab
	s_add_i32 s10, s53, 0x357
	s_bfe_u32 s10, s10, 0x70009
	s_mul_i32 s10, s10, 3
	s_sub_i32 s10, s37, s10
	s_add_i32 s10, s10, 5
	s_and_b32 s10, s10, 0xff
	s_lshl_b32 s10, s10, 14
	s_add_i32 s56, s39, s10
	s_add_i32 s52, s37, 2
	s_waitcnt vmcnt(4)
	s_sub_i32 s10, s36, 32
	v_cvt_pk_bf16_f32 v34, v34, v38
	s_cmp_lt_u32 s52, 61
	ds_write_b32 v169, v34 offset:57344
	v_cvt_pk_bf16_f32 v34, v35, v39
	s_cselect_b32 s10, s10, 0x7e0
	ds_write_b32 v169, v34 offset:57408
	v_cvt_pk_bf16_f32 v34, v36, v40
	s_lshl_b64 s[54:55], s[10:11], 11
	ds_write_b32 v169, v34 offset:57472
	v_cvt_pk_bf16_f32 v34, v37, v41
	ds_write_b32 v169, v34 offset:57536
	v_lshl_add_u64 v[38:39], v[156:157], 0, s[54:55]
	global_load_dwordx4 v[34:37], v[38:39], off sc1 nt
	v_lshl_add_u64 v[38:39], v[38:39], 0, s[22:23]
	global_load_dwordx4 v[38:41], v[38:39], off sc1 nt
	v_add_u32_e32 v93, s56, v160
	v_add_u32_e32 v52, v93, v163
	v_add_u32_e32 v92, v161, v162
	ds_read_b64 v[64:65], v52
	ds_read_b128 v[52:55], v92 offset:49152
	ds_read_b128 v[56:59], v92 offset:51200
	ds_read_b128 v[60:63], v92 offset:53248
	ds_read_b128 v[82:85], v92 offset:55296
	s_waitcnt lgkmcnt(0)
	v_cvt_pk_f32_fp8_e32 v[86:87], v64
	v_cvt_pk_f32_fp8_sdwa v[88:89], v64 src0_sel:WORD_1
	v_cvt_pk_f32_fp8_e32 v[90:91], v65
	v_cvt_pk_f32_fp8_sdwa v[64:65], v65 src0_sel:WORD_1
	v_cvt_pk_bf16_f32 v86, v86, v87
	v_cvt_pk_bf16_f32 v87, v88, v89
	v_cvt_pk_bf16_f32 v88, v90, v91
	v_cvt_pk_bf16_f32 v89, v64, v65
	s_nop 1
	v_mfma_f32_32x32x16_bf16 v[114:129], v[52:55], v[86:89], v[114:129]
	v_mfma_f32_32x32x16_bf16 v[18:33], v[56:59], v[86:89], v[18:33]
	v_mfma_f32_32x32x16_bf16 v[66:81], v[60:63], v[86:89], v[66:81]
	v_mfma_f32_32x32x16_bf16 v[2:17], v[82:85], v[86:89], v[2:17]
	v_add_u32_e32 v52, v93, v165
	v_add_u32_e32 v94, v161, v164
	ds_read_b64 v[64:65], v52
	ds_read_b128 v[52:55], v94 offset:49152
	ds_read_b128 v[56:59], v94 offset:51200
	ds_read_b128 v[60:63], v94 offset:53248
	ds_read_b128 v[82:85], v94 offset:55296
	s_waitcnt lgkmcnt(0)
	v_cvt_pk_f32_fp8_e32 v[86:87], v64
	v_cvt_pk_f32_fp8_sdwa v[88:89], v64 src0_sel:WORD_1
	v_cvt_pk_f32_fp8_e32 v[90:91], v65
	v_cvt_pk_f32_fp8_sdwa v[64:65], v65 src0_sel:WORD_1
	v_cvt_pk_bf16_f32 v86, v86, v87
	v_cvt_pk_bf16_f32 v87, v88, v89
	v_cvt_pk_bf16_f32 v88, v90, v91
	v_cvt_pk_bf16_f32 v89, v64, v65
	s_nop 0
	v_mfma_f32_32x32x16_bf16 v[114:129], v[52:55], v[86:89], v[114:129]
	v_mfma_f32_32x32x16_bf16 v[18:33], v[56:59], v[86:89], v[18:33]
	v_mfma_f32_32x32x16_bf16 v[66:81], v[60:63], v[86:89], v[66:81]
	v_mfma_f32_32x32x16_bf16 v[2:17], v[82:85], v[86:89], v[2:17]
	s_waitcnt vmcnt(5)
	s_mov_b32 m0, s56
	s_waitcnt lgkmcnt(0)
	s_barrier
	v_lshl_add_u64 v[52:53], v[50:51], 0, s[10:11]
	global_load_lds_dwordx4 v[52:53], off
	s_addk_i32 s53, 0x402
	s_bfe_u32 s10, s53, 0x70009
	s_mul_i32 s10, s10, 3
	s_sub_i32 s10, s37, s10
	s_add_i32 s10, s10, 6
	s_and_b32 s10, s10, 0xff
	s_lshl_b32 s10, s10, 14
	s_add_i32 s37, s39, s10
	s_waitcnt vmcnt(4)
	s_cmp_lt_u32 s52, 60
	v_cvt_pk_bf16_f32 v42, v42, v46
	ds_write_b32 v169, v42 offset:49152
	v_cvt_pk_bf16_f32 v42, v43, v47
	s_cselect_b32 s10, s36, 0x7e0
	ds_write_b32 v169, v42 offset:49216
	v_cvt_pk_bf16_f32 v42, v44, v48
	s_lshl_b64 s[54:55], s[10:11], 11
	ds_write_b32 v169, v42 offset:49280
	v_cvt_pk_bf16_f32 v42, v45, v49
	ds_write_b32 v169, v42 offset:49344
	v_lshl_add_u64 v[46:47], v[156:157], 0, s[54:55]
	global_load_dwordx4 v[42:45], v[46:47], off sc1 nt
	v_lshl_add_u64 v[46:47], v[46:47], 0, s[22:23]
	global_load_dwordx4 v[46:49], v[46:47], off sc1 nt
	v_add_u32_e32 v93, s37, v160
	v_add_u32_e32 v52, v93, v163
	ds_read_b64 v[64:65], v52
	ds_read_b128 v[52:55], v92 offset:57344
	ds_read_b128 v[56:59], v92 offset:59392
	ds_read_b128 v[60:63], v92 offset:61440
	ds_read_b128 v[82:85], v92 offset:63488
	s_waitcnt lgkmcnt(0)
	v_cvt_pk_f32_fp8_e32 v[86:87], v64
	v_cvt_pk_f32_fp8_sdwa v[88:89], v64 src0_sel:WORD_1
	v_cvt_pk_f32_fp8_e32 v[90:91], v65
	v_cvt_pk_f32_fp8_sdwa v[64:65], v65 src0_sel:WORD_1
	v_cvt_pk_bf16_f32 v86, v86, v87
	v_cvt_pk_bf16_f32 v87, v88, v89
	v_cvt_pk_bf16_f32 v88, v90, v91
	v_cvt_pk_bf16_f32 v89, v64, v65
	s_nop 1
	v_mfma_f32_32x32x16_bf16 v[114:129], v[52:55], v[86:89], v[114:129]
	v_mfma_f32_32x32x16_bf16 v[18:33], v[56:59], v[86:89], v[18:33]
	v_mfma_f32_32x32x16_bf16 v[66:81], v[60:63], v[86:89], v[66:81]
	v_mfma_f32_32x32x16_bf16 v[2:17], v[82:85], v[86:89], v[2:17]
	v_add_u32_e32 v52, v93, v165
	ds_read_b64 v[64:65], v52
	ds_read_b128 v[52:55], v94 offset:57344
	ds_read_b128 v[56:59], v94 offset:59392
	ds_read_b128 v[60:63], v94 offset:61440
	ds_read_b128 v[82:85], v94 offset:63488
	s_waitcnt lgkmcnt(0)
	v_cvt_pk_f32_fp8_e32 v[86:87], v64
	v_cvt_pk_f32_fp8_sdwa v[88:89], v64 src0_sel:WORD_1
	v_cvt_pk_f32_fp8_e32 v[90:91], v65
	v_cvt_pk_f32_fp8_sdwa v[64:65], v65 src0_sel:WORD_1
	v_cvt_pk_bf16_f32 v86, v86, v87
	v_cvt_pk_bf16_f32 v87, v88, v89
	v_cvt_pk_bf16_f32 v88, v90, v91
	v_cvt_pk_bf16_f32 v89, v64, v65
	s_nop 0
	v_mfma_f32_32x32x16_bf16 v[114:129], v[52:55], v[86:89], v[114:129]
	v_mfma_f32_32x32x16_bf16 v[18:33], v[56:59], v[86:89], v[18:33]
	v_mfma_f32_32x32x16_bf16 v[66:81], v[60:63], v[86:89], v[66:81]
	v_mfma_f32_32x32x16_bf16 v[2:17], v[82:85], v[86:89], v[2:17]
	s_waitcnt vmcnt(5)
	s_mov_b32 m0, s37
	s_waitcnt lgkmcnt(0)
	s_barrier
	v_lshl_add_u64 v[52:53], v[50:51], 0, s[10:11]
	global_load_lds_dwordx4 v[52:53], off
	s_add_i32 s36, s36, 64
	s_cmp_gt_u32 s52, 61
	s_mov_b32 s37, s52
	s_cbranch_scc0 .Lmoe_B_1015
.Lmoe_X_1015:
	s_waitcnt vmcnt(0)
	s_mov_b64 s[36:37], 0
.LBB0_1017:
	v_mov_b32_e32 v97, 0
	s_and_b64 vcc, exec, s[36:37]
	v_mov_b32_e32 v96, v97
	v_mov_b32_e32 v95, v97
	v_mov_b32_e32 v94, v97
	v_mov_b32_e32 v93, v97
	v_mov_b32_e32 v92, v97
	v_mov_b32_e32 v91, v97
	v_mov_b32_e32 v90, v97
	v_mov_b32_e32 v89, v97
	v_mov_b32_e32 v88, v97
	v_mov_b32_e32 v87, v97
	v_mov_b32_e32 v86, v97
	v_mov_b32_e32 v85, v97
	v_mov_b32_e32 v84, v97
	v_mov_b32_e32 v83, v97
	v_mov_b32_e32 v82, v97
	v_mov_b32_e32 v65, v97
	v_mov_b32_e32 v64, v97
	v_mov_b32_e32 v63, v97
	v_mov_b32_e32 v62, v97
	v_mov_b32_e32 v61, v97
	v_mov_b32_e32 v60, v97
	v_mov_b32_e32 v59, v97
	v_mov_b32_e32 v58, v97
	v_mov_b32_e32 v57, v97
	v_mov_b32_e32 v56, v97
	v_mov_b32_e32 v55, v97
	v_mov_b32_e32 v54, v97
	v_mov_b32_e32 v53, v97
	v_mov_b32_e32 v52, v97
	v_mov_b32_e32 v51, v97
	v_mov_b32_e32 v50, v97
	v_mov_b32_e32 v113, v97
	v_mov_b32_e32 v112, v97
	v_mov_b32_e32 v111, v97
	v_mov_b32_e32 v110, v97
	v_mov_b32_e32 v109, v97
	v_mov_b32_e32 v108, v97
	v_mov_b32_e32 v107, v97
	v_mov_b32_e32 v106, v97
	v_mov_b32_e32 v105, v97
	v_mov_b32_e32 v104, v97
	v_mov_b32_e32 v103, v97
	v_mov_b32_e32 v102, v97
	v_mov_b32_e32 v101, v97
	v_mov_b32_e32 v100, v97
	v_mov_b32_e32 v99, v97
	v_mov_b32_e32 v98, v97
	v_mov_b32_e32 v49, v97
	v_mov_b32_e32 v48, v97
	v_mov_b32_e32 v47, v97
	v_mov_b32_e32 v46, v97
	v_mov_b32_e32 v45, v97
	v_mov_b32_e32 v44, v97
	v_mov_b32_e32 v43, v97
	v_mov_b32_e32 v42, v97
	v_mov_b32_e32 v41, v97
	v_mov_b32_e32 v40, v97
	v_mov_b32_e32 v39, v97
	v_mov_b32_e32 v38, v97
	v_mov_b32_e32 v37, v97
	v_mov_b32_e32 v36, v97
	v_mov_b32_e32 v35, v97
	v_mov_b32_e32 v34, v97
	s_cbranch_vccz .LBB0_1021
	global_load_dwordx4 v[2:5], v[156:157], off sc1 nt
	s_mov_b32 m0, s39
	global_load_dwordx4 v[6:9], v[132:133], off sc1 nt
	v_or_b32_e32 v158, v136, v1
	global_load_lds_dwordx4 v146, s[14:15]
	s_mov_b32 m0, s42
	v_mov_b32_e32 v159, v147
	global_load_lds_dwordx4 v158, s[14:15]
	global_load_dwordx4 v[130:133], v[130:131], off sc1 nt
	global_load_dwordx4 v[134:137], v[134:135], off sc1 nt
	s_mov_b32 m0, s40
	s_nop 0
	global_load_lds_dwordx4 v146, s[16:17]
	s_mov_b32 m0, s43
	s_nop 0
	global_load_lds_dwordx4 v158, s[16:17]
	s_waitcnt vmcnt(6)
	s_nop 0
	v_cvt_pk_bf16_f32 v2, v2, v6
	ds_write_b32 v169, v2 offset:49152
	v_cvt_pk_bf16_f32 v2, v3, v7
	ds_write_b32 v169, v2 offset:49216
	v_cvt_pk_bf16_f32 v2, v4, v8
	ds_write_b32 v169, v2 offset:49280
	v_cvt_pk_bf16_f32 v2, v5, v9
	ds_write_b32 v169, v2 offset:49344
	global_load_dwordx4 v[138:141], v[138:139], off sc1 nt
	global_load_dwordx4 v[142:145], v[142:143], off sc1 nt
	s_waitcnt vmcnt(6)
	s_mov_b32 m0, s41
	s_waitcnt lgkmcnt(0)
	s_barrier
	global_load_lds_dwordx4 v146, s[18:19]
	s_mov_b32 m0, s44
	v_mov_b32_e32 v34, 0
	global_load_lds_dwordx4 v158, s[18:19]
	s_mov_b32 s37, -2
	s_movk_i32 s36, 0x80
	v_mov_b32_e32 v35, v34
	v_mov_b32_e32 v36, v34
	v_mov_b32_e32 v37, v34
	v_mov_b32_e32 v38, v34
	v_mov_b32_e32 v39, v34
	v_mov_b32_e32 v40, v34
	v_mov_b32_e32 v41, v34
	v_mov_b32_e32 v42, v34
	v_mov_b32_e32 v43, v34
	v_mov_b32_e32 v44, v34
	v_mov_b32_e32 v45, v34
	v_mov_b32_e32 v46, v34
	v_mov_b32_e32 v47, v34
	v_mov_b32_e32 v48, v34
	v_mov_b32_e32 v49, v34
	v_mov_b32_e32 v98, v34
	v_mov_b32_e32 v99, v34
	v_mov_b32_e32 v100, v34
	v_mov_b32_e32 v101, v34
	v_mov_b32_e32 v102, v34
	v_mov_b32_e32 v103, v34
	v_mov_b32_e32 v104, v34
	v_mov_b32_e32 v105, v34
	v_mov_b32_e32 v106, v34
	v_mov_b32_e32 v107, v34
	v_mov_b32_e32 v108, v34
	v_mov_b32_e32 v109, v34
	v_mov_b32_e32 v110, v34
	v_mov_b32_e32 v111, v34
	v_mov_b32_e32 v112, v34
	v_mov_b32_e32 v113, v34
	v_mov_b32_e32 v50, v34
	v_mov_b32_e32 v51, v34
	v_mov_b32_e32 v52, v34
	v_mov_b32_e32 v53, v34
	v_mov_b32_e32 v54, v34
	v_mov_b32_e32 v55, v34
	v_mov_b32_e32 v56, v34
	v_mov_b32_e32 v57, v34
	v_mov_b32_e32 v58, v34
	v_mov_b32_e32 v59, v34
	v_mov_b32_e32 v60, v34
	v_mov_b32_e32 v61, v34
	v_mov_b32_e32 v62, v34
	v_mov_b32_e32 v63, v34
	v_mov_b32_e32 v64, v34
	v_mov_b32_e32 v65, v34
	v_mov_b32_e32 v82, v34
	v_mov_b32_e32 v83, v34
	v_mov_b32_e32 v84, v34
	v_mov_b32_e32 v85, v34
	v_mov_b32_e32 v86, v34
	v_mov_b32_e32 v87, v34
	v_mov_b32_e32 v88, v34
	v_mov_b32_e32 v89, v34
	v_mov_b32_e32 v90, v34
	v_mov_b32_e32 v91, v34
	v_mov_b32_e32 v92, v34
	v_mov_b32_e32 v93, v34
	v_mov_b32_e32 v94, v34
	v_mov_b32_e32 v95, v34
	v_mov_b32_e32 v96, v34
	v_mov_b32_e32 v97, v34
	v_mov_b32_e32 v2, v34
	v_mov_b32_e32 v3, v34
	v_mov_b32_e32 v4, v34
	v_mov_b32_e32 v5, v34
	v_mov_b32_e32 v6, v34
	v_mov_b32_e32 v7, v34
	v_mov_b32_e32 v8, v34
	v_mov_b32_e32 v9, v34
	v_mov_b32_e32 v10, v34
	v_mov_b32_e32 v11, v34
	v_mov_b32_e32 v12, v34
	v_mov_b32_e32 v13, v34
	v_mov_b32_e32 v14, v34
	v_mov_b32_e32 v15, v34
	v_mov_b32_e32 v16, v34
	v_mov_b32_e32 v17, v34
	v_mov_b32_e32 v66, v34
	v_mov_b32_e32 v67, v34
	v_mov_b32_e32 v68, v34
	v_mov_b32_e32 v69, v34
	v_mov_b32_e32 v70, v34
	v_mov_b32_e32 v71, v34
	v_mov_b32_e32 v72, v34
	v_mov_b32_e32 v73, v34
	v_mov_b32_e32 v74, v34
	v_mov_b32_e32 v75, v34
	v_mov_b32_e32 v76, v34
	v_mov_b32_e32 v77, v34
	v_mov_b32_e32 v78, v34
	v_mov_b32_e32 v79, v34
	v_mov_b32_e32 v80, v34
	v_mov_b32_e32 v81, v34
	v_mov_b32_e32 v18, v34
	v_mov_b32_e32 v19, v34
	v_mov_b32_e32 v20, v34
	v_mov_b32_e32 v21, v34
	v_mov_b32_e32 v22, v34
	v_mov_b32_e32 v23, v34
	v_mov_b32_e32 v24, v34
	v_mov_b32_e32 v25, v34
	v_mov_b32_e32 v26, v34
	v_mov_b32_e32 v27, v34
	v_mov_b32_e32 v28, v34
	v_mov_b32_e32 v29, v34
	v_mov_b32_e32 v30, v34
	v_mov_b32_e32 v31, v34
	v_mov_b32_e32 v32, v34
	v_mov_b32_e32 v33, v34
	v_mov_b32_e32 v114, v34
	v_mov_b32_e32 v115, v34
	v_mov_b32_e32 v116, v34
	v_mov_b32_e32 v117, v34
	v_mov_b32_e32 v118, v34
	v_mov_b32_e32 v119, v34
	v_mov_b32_e32 v120, v34
	v_mov_b32_e32 v121, v34
	v_mov_b32_e32 v122, v34
	v_mov_b32_e32 v123, v34
	v_mov_b32_e32 v124, v34
	v_mov_b32_e32 v125, v34
	v_mov_b32_e32 v126, v34
	v_mov_b32_e32 v127, v34
	v_mov_b32_e32 v128, v34
	v_mov_b32_e32 v129, v34
	v_readfirstlane_b32 s98, v250
	s_bitcmp1_b32 s98, 8
	s_cbranch_scc1 .Lmoe_B_1019
.LBB0_1019:
	s_mul_i32 s53, s37, 0xab
	s_add_i32 s10, s53, 0x357
	s_bfe_u32 s10, s10, 0x70009
	s_mul_i32 s10, s10, 3
	s_sub_i32 s10, s37, s10
	s_add_i32 s10, s10, 5
	s_and_b32 s10, s10, 0xff
	s_lshl_b32 s10, s10, 14
	s_add_i32 s54, s39, s10
	s_add_i32 s52, s37, 2
	v_add_u32_e32 v171, s54, v160
	v_add_u32_e32 v198, v171, v163
	v_add_u32_e32 v154, v161, v162
	ds_read_b64 v[188:189], v198
	ds_read_b128 v[172:175], v154 offset:49152
	ds_read_b128 v[176:179], v154 offset:51200
	ds_read_b128 v[180:183], v154 offset:53248
	ds_read_b128 v[184:187], v154 offset:55296
	s_waitcnt lgkmcnt(0)
	v_cvt_pk_f32_fp8_e32 v[190:191], v188
	v_cvt_pk_f32_fp8_sdwa v[192:193], v188 src0_sel:WORD_1
	v_cvt_pk_f32_fp8_e32 v[194:195], v189
	v_cvt_pk_f32_fp8_sdwa v[196:197], v189 src0_sel:WORD_1
	v_cvt_pk_bf16_f32 v188, v190, v191
	v_cvt_pk_bf16_f32 v189, v192, v193
	v_cvt_pk_bf16_f32 v190, v194, v195
	v_cvt_pk_bf16_f32 v191, v196, v197
	ds_read_b64 v[192:193], v198 offset:8192
	s_waitcnt lgkmcnt(0)
	v_cvt_pk_f32_fp8_e32 v[194:195], v192
	v_cvt_pk_f32_fp8_sdwa v[196:197], v192 src0_sel:WORD_1
	v_cvt_pk_f32_fp8_e32 v[198:199], v193
	v_cvt_pk_f32_fp8_sdwa v[200:201], v193 src0_sel:WORD_1
	v_cvt_pk_bf16_f32 v192, v194, v195
	v_cvt_pk_bf16_f32 v193, v196, v197
	v_cvt_pk_bf16_f32 v194, v198, v199
	v_cvt_pk_bf16_f32 v195, v200, v201
	s_waitcnt vmcnt(6)
	s_sub_i32 s10, s36, 32
	v_cvt_pk_bf16_f32 v130, v130, v134
	s_cmp_lt_u32 s52, 61
	ds_write_b32 v169, v130 offset:57344
	v_cvt_pk_bf16_f32 v130, v131, v135
	s_cselect_b32 s10, s10, 0x7e0
	ds_write_b32 v169, v130 offset:57408
	v_cvt_pk_bf16_f32 v130, v132, v136
	s_lshl_b64 s[56:57], s[10:11], 11
	ds_write_b32 v169, v130 offset:57472
	v_cvt_pk_bf16_f32 v130, v133, v137
	ds_write_b32 v169, v130 offset:57536
	v_lshl_add_u64 v[134:135], v[156:157], 0, s[56:57]
	global_load_dwordx4 v[130:133], v[134:135], off sc1 nt
	v_lshl_add_u64 v[134:135], v[134:135], 0, s[22:23]
	global_load_dwordx4 v[134:137], v[134:135], off sc1 nt
	v_mfma_f32_32x32x16_bf16 v[114:129], v[172:175], v[188:191], v[114:129]
	v_mfma_f32_32x32x16_bf16 v[18:33], v[176:179], v[188:191], v[18:33]
	v_mfma_f32_32x32x16_bf16 v[66:81], v[180:183], v[188:191], v[66:81]
	v_mfma_f32_32x32x16_bf16 v[2:17], v[184:187], v[188:191], v[2:17]
	v_mfma_f32_32x32x16_bf16 v[82:97], v[172:175], v[192:195], v[82:97]
	v_mfma_f32_32x32x16_bf16 v[50:65], v[176:179], v[192:195], v[50:65]
	v_mfma_f32_32x32x16_bf16 v[98:113], v[180:183], v[192:195], v[98:113]
	v_mfma_f32_32x32x16_bf16 v[34:49], v[184:187], v[192:195], v[34:49]
	v_add_u32_e32 v171, v171, v165
	v_add_u32_e32 v202, v161, v164
	ds_read_b64 v[188:189], v171
	ds_read_b128 v[172:175], v202 offset:49152
	ds_read_b128 v[176:179], v202 offset:51200
	ds_read_b128 v[180:183], v202 offset:53248
	ds_read_b128 v[184:187], v202 offset:55296
	s_waitcnt lgkmcnt(0)
	v_cvt_pk_f32_fp8_e32 v[190:191], v188
	v_cvt_pk_f32_fp8_sdwa v[192:193], v188 src0_sel:WORD_1
	v_cvt_pk_f32_fp8_e32 v[194:195], v189
	v_cvt_pk_f32_fp8_sdwa v[196:197], v189 src0_sel:WORD_1
	v_cvt_pk_bf16_f32 v188, v190, v191
	v_cvt_pk_bf16_f32 v189, v192, v193
	v_cvt_pk_bf16_f32 v190, v194, v195
	v_cvt_pk_bf16_f32 v191, v196, v197
	ds_read_b64 v[192:193], v171 offset:8192
	v_mfma_f32_32x32x16_bf16 v[114:129], v[172:175], v[188:191], v[114:129]
	s_waitcnt lgkmcnt(0)
	v_cvt_pk_f32_fp8_e32 v[194:195], v192
	v_cvt_pk_f32_fp8_e32 v[196:197], v193
	v_mfma_f32_32x32x16_bf16 v[18:33], v[176:179], v[188:191], v[18:33]
	v_mfma_f32_32x32x16_bf16 v[66:81], v[180:183], v[188:191], v[66:81]
	v_mfma_f32_32x32x16_bf16 v[2:17], v[184:187], v[188:191], v[2:17]
	v_cvt_pk_f32_fp8_sdwa v[190:191], v192 src0_sel:WORD_1
	v_cvt_pk_f32_fp8_sdwa v[192:193], v193 src0_sel:WORD_1
	v_cvt_pk_bf16_f32 v188, v194, v195
	v_cvt_pk_bf16_f32 v189, v190, v191
	v_cvt_pk_bf16_f32 v190, v196, v197
	v_cvt_pk_bf16_f32 v191, v192, v193
	s_nop 0
	v_mfma_f32_32x32x16_bf16 v[82:97], v[172:175], v[188:191], v[82:97]
	v_mfma_f32_32x32x16_bf16 v[50:65], v[176:179], v[188:191], v[50:65]
	v_mfma_f32_32x32x16_bf16 v[98:113], v[180:183], v[188:191], v[98:113]
	v_mfma_f32_32x32x16_bf16 v[34:49], v[184:187], v[188:191], v[34:49]
	s_add_u32 s56, s14, s10
	s_waitcnt vmcnt(6)
	s_addc_u32 s57, s15, 0
	s_mov_b32 m0, s54
	s_waitcnt lgkmcnt(0)
	s_barrier
	v_lshl_add_u64 v[172:173], s[56:57], 0, v[146:147]
	global_load_lds_dwordx4 v[172:173], off
	v_lshl_add_u64 v[172:173], s[56:57], 0, v[158:159]
	s_add_i32 m0, s54, 0x2000
	s_addk_i32 s53, 0x402
	global_load_lds_dwordx4 v[172:173], off
	s_bfe_u32 s10, s53, 0x70009
	s_mul_i32 s10, s10, 3
	s_sub_i32 s10, s37, s10
	s_add_i32 s10, s10, 6
	s_and_b32 s10, s10, 0xff
	s_lshl_b32 s10, s10, 14
	s_add_i32 s37, s39, s10
	v_add_u32_e32 v171, s37, v160
	v_add_u32_e32 v198, v171, v163
	ds_read_b64 v[188:189], v198
	ds_read_b128 v[172:175], v154 offset:57344
	ds_read_b128 v[176:179], v154 offset:59392
	ds_read_b128 v[180:183], v154 offset:61440
	ds_read_b128 v[184:187], v154 offset:63488
	s_waitcnt lgkmcnt(0)
	v_cvt_pk_f32_fp8_e32 v[190:191], v188
	v_cvt_pk_f32_fp8_sdwa v[192:193], v188 src0_sel:WORD_1
	v_cvt_pk_f32_fp8_e32 v[194:195], v189
	v_cvt_pk_f32_fp8_sdwa v[196:197], v189 src0_sel:WORD_1
	v_cvt_pk_bf16_f32 v188, v190, v191
	v_cvt_pk_bf16_f32 v189, v192, v193
	v_cvt_pk_bf16_f32 v190, v194, v195
	v_cvt_pk_bf16_f32 v191, v196, v197
	ds_read_b64 v[192:193], v198 offset:8192
	s_waitcnt lgkmcnt(0)
	v_cvt_pk_f32_fp8_e32 v[194:195], v192
	v_cvt_pk_f32_fp8_sdwa v[196:197], v192 src0_sel:WORD_1
	v_cvt_pk_f32_fp8_e32 v[198:199], v193
	v_cvt_pk_f32_fp8_sdwa v[200:201], v193 src0_sel:WORD_1
	v_cvt_pk_bf16_f32 v192, v194, v195
	v_cvt_pk_bf16_f32 v193, v196, v197
	v_cvt_pk_bf16_f32 v194, v198, v199
	v_cvt_pk_bf16_f32 v195, v200, v201
	s_waitcnt vmcnt(6)
	s_cmp_lt_u32 s52, 60
	v_cvt_pk_bf16_f32 v138, v138, v142
	ds_write_b32 v169, v138 offset:49152
	v_cvt_pk_bf16_f32 v138, v139, v143
	s_cselect_b32 s10, s36, 0x7e0
	ds_write_b32 v169, v138 offset:49216
	v_cvt_pk_bf16_f32 v138, v140, v144
	s_lshl_b64 s[54:55], s[10:11], 11
	ds_write_b32 v169, v138 offset:49280
	v_cvt_pk_bf16_f32 v138, v141, v145
	ds_write_b32 v169, v138 offset:49344
	v_lshl_add_u64 v[142:143], v[156:157], 0, s[54:55]
	global_load_dwordx4 v[138:141], v[142:143], off sc1 nt
	v_lshl_add_u64 v[142:143], v[142:143], 0, s[22:23]
	global_load_dwordx4 v[142:145], v[142:143], off sc1 nt
	v_mfma_f32_32x32x16_bf16 v[114:129], v[172:175], v[188:191], v[114:129]
	v_mfma_f32_32x32x16_bf16 v[18:33], v[176:179], v[188:191], v[18:33]
	v_mfma_f32_32x32x16_bf16 v[66:81], v[180:183], v[188:191], v[66:81]
	v_mfma_f32_32x32x16_bf16 v[2:17], v[184:187], v[188:191], v[2:17]
	v_mfma_f32_32x32x16_bf16 v[82:97], v[172:175], v[192:195], v[82:97]
	v_mfma_f32_32x32x16_bf16 v[50:65], v[176:179], v[192:195], v[50:65]
	v_mfma_f32_32x32x16_bf16 v[98:113], v[180:183], v[192:195], v[98:113]
	v_mfma_f32_32x32x16_bf16 v[34:49], v[184:187], v[192:195], v[34:49]
	v_add_u32_e32 v154, v171, v165
	ds_read_b64 v[188:189], v154
	ds_read_b128 v[172:175], v202 offset:57344
	ds_read_b128 v[176:179], v202 offset:59392
	ds_read_b128 v[180:183], v202 offset:61440
	ds_read_b128 v[184:187], v202 offset:63488
	s_waitcnt lgkmcnt(0)
	v_cvt_pk_f32_fp8_e32 v[190:191], v188
	v_cvt_pk_f32_fp8_sdwa v[192:193], v188 src0_sel:WORD_1
	v_cvt_pk_f32_fp8_e32 v[194:195], v189
	v_cvt_pk_f32_fp8_sdwa v[196:197], v189 src0_sel:WORD_1
	v_cvt_pk_bf16_f32 v188, v190, v191
	v_cvt_pk_bf16_f32 v189, v192, v193
	v_cvt_pk_bf16_f32 v190, v194, v195
	v_cvt_pk_bf16_f32 v191, v196, v197
	ds_read_b64 v[192:193], v154 offset:8192
	v_mfma_f32_32x32x16_bf16 v[114:129], v[172:175], v[188:191], v[114:129]
	s_waitcnt lgkmcnt(0)
	v_cvt_pk_f32_fp8_e32 v[194:195], v192
	v_cvt_pk_f32_fp8_e32 v[196:197], v193
	v_mfma_f32_32x32x16_bf16 v[18:33], v[176:179], v[188:191], v[18:33]
	v_mfma_f32_32x32x16_bf16 v[66:81], v[180:183], v[188:191], v[66:81]
	v_mfma_f32_32x32x16_bf16 v[2:17], v[184:187], v[188:191], v[2:17]
	v_cvt_pk_f32_fp8_sdwa v[190:191], v192 src0_sel:WORD_1
	v_cvt_pk_f32_fp8_sdwa v[192:193], v193 src0_sel:WORD_1
	v_cvt_pk_bf16_f32 v188, v194, v195
	v_cvt_pk_bf16_f32 v189, v190, v191
	v_cvt_pk_bf16_f32 v190, v196, v197
	v_cvt_pk_bf16_f32 v191, v192, v193
	s_nop 0
	v_mfma_f32_32x32x16_bf16 v[82:97], v[172:175], v[188:191], v[82:97]
	v_mfma_f32_32x32x16_bf16 v[50:65], v[176:179], v[188:191], v[50:65]
	v_mfma_f32_32x32x16_bf16 v[98:113], v[180:183], v[188:191], v[98:113]
	v_mfma_f32_32x32x16_bf16 v[34:49], v[184:187], v[188:191], v[34:49]
	s_add_u32 s54, s14, s10
	s_waitcnt vmcnt(6)
	s_addc_u32 s55, s15, 0
	s_mov_b32 m0, s37
	s_waitcnt lgkmcnt(0)
	s_barrier
	v_lshl_add_u64 v[172:173], s[54:55], 0, v[146:147]
	global_load_lds_dwordx4 v[172:173], off
	v_lshl_add_u64 v[172:173], s[54:55], 0, v[158:159]
	s_add_i32 m0, s37, 0x2000
	s_add_i32 s36, s36, 64
	global_load_lds_dwordx4 v[172:173], off
	s_cmp_gt_u32 s52, 61
	s_mov_b32 s37, s52
	s_cbranch_scc0 .LBB0_1019
	s_branch .Lmoe_X_1019
.Lmoe_B_1019:
	s_mul_i32 s53, s37, 0xab
	s_add_i32 s10, s53, 0x357
	s_bfe_u32 s10, s10, 0x70009
	s_mul_i32 s10, s10, 3
	s_sub_i32 s10, s37, s10
	s_add_i32 s10, s10, 5
	s_and_b32 s10, s10, 0xff
	s_lshl_b32 s10, s10, 14
	s_add_i32 s54, s39, s10
	s_add_i32 s52, s37, 2
	s_waitcnt vmcnt(6)
	s_sub_i32 s10, s36, 32
	v_cvt_pk_bf16_f32 v130, v130, v134
	s_cmp_lt_u32 s52, 61
	ds_write_b32 v169, v130 offset:57344
	v_cvt_pk_bf16_f32 v130, v131, v135
	s_cselect_b32 s10, s10, 0x7e0
	ds_write_b32 v169, v130 offset:57408
	v_cvt_pk_bf16_f32 v130, v132, v136
	s_lshl_b64 s[56:57], s[10:11], 11
	ds_write_b32 v169, v130 offset:57472
	v_cvt_pk_bf16_f32 v130, v133, v137
	ds_write_b32 v169, v130 offset:57536
	v_lshl_add_u64 v[134:135], v[156:157], 0, s[56:57]
	global_load_dwordx4 v[130:133], v[134:135], off sc1 nt
	v_lshl_add_u64 v[134:135], v[134:135], 0, s[22:23]
	global_load_dwordx4 v[134:137], v[134:135], off sc1 nt
	v_add_u32_e32 v171, s54, v160
	v_add_u32_e32 v198, v171, v163
	v_add_u32_e32 v154, v161, v162
	ds_read_b64 v[188:189], v198
	ds_read_b128 v[172:175], v154 offset:49152
	ds_read_b128 v[176:179], v154 offset:51200
	ds_read_b128 v[180:183], v154 offset:53248
	ds_read_b128 v[184:187], v154 offset:55296
	s_waitcnt lgkmcnt(0)
	v_cvt_pk_f32_fp8_e32 v[190:191], v188
	v_cvt_pk_f32_fp8_sdwa v[192:193], v188 src0_sel:WORD_1
	v_cvt_pk_f32_fp8_e32 v[194:195], v189
	v_cvt_pk_f32_fp8_sdwa v[196:197], v189 src0_sel:WORD_1
	v_cvt_pk_bf16_f32 v188, v190, v191
	v_cvt_pk_bf16_f32 v189, v192, v193
	v_cvt_pk_bf16_f32 v190, v194, v195
	v_cvt_pk_bf16_f32 v191, v196, v197
	ds_read_b64 v[192:193], v198 offset:8192
	s_waitcnt lgkmcnt(0)
	v_cvt_pk_f32_fp8_e32 v[194:195], v192
	v_cvt_pk_f32_fp8_sdwa v[196:197], v192 src0_sel:WORD_1
	v_cvt_pk_f32_fp8_e32 v[198:199], v193
	v_cvt_pk_f32_fp8_sdwa v[200:201], v193 src0_sel:WORD_1
	v_cvt_pk_bf16_f32 v192, v194, v195
	v_cvt_pk_bf16_f32 v193, v196, v197
	v_cvt_pk_bf16_f32 v194, v198, v199
	v_cvt_pk_bf16_f32 v195, v200, v201
	s_nop 1
	v_mfma_f32_32x32x16_bf16 v[114:129], v[172:175], v[188:191], v[114:129]
	v_mfma_f32_32x32x16_bf16 v[18:33], v[176:179], v[188:191], v[18:33]
	v_mfma_f32_32x32x16_bf16 v[66:81], v[180:183], v[188:191], v[66:81]
	v_mfma_f32_32x32x16_bf16 v[2:17], v[184:187], v[188:191], v[2:17]
	v_mfma_f32_32x32x16_bf16 v[82:97], v[172:175], v[192:195], v[82:97]
	v_mfma_f32_32x32x16_bf16 v[50:65], v[176:179], v[192:195], v[50:65]
	v_mfma_f32_32x32x16_bf16 v[98:113], v[180:183], v[192:195], v[98:113]
	v_mfma_f32_32x32x16_bf16 v[34:49], v[184:187], v[192:195], v[34:49]
	v_add_u32_e32 v171, v171, v165
	v_add_u32_e32 v202, v161, v164
	ds_read_b64 v[188:189], v171
	ds_read_b128 v[172:175], v202 offset:49152
	ds_read_b128 v[176:179], v202 offset:51200
	ds_read_b128 v[180:183], v202 offset:53248
	ds_read_b128 v[184:187], v202 offset:55296
	s_waitcnt lgkmcnt(0)
	v_cvt_pk_f32_fp8_e32 v[190:191], v188
	v_cvt_pk_f32_fp8_sdwa v[192:193], v188 src0_sel:WORD_1
	v_cvt_pk_f32_fp8_e32 v[194:195], v189
	v_cvt_pk_f32_fp8_sdwa v[196:197], v189 src0_sel:WORD_1
	v_cvt_pk_bf16_f32 v188, v190, v191
	v_cvt_pk_bf16_f32 v189, v192, v193
	v_cvt_pk_bf16_f32 v190, v194, v195
	v_cvt_pk_bf16_f32 v191, v196, v197
	ds_read_b64 v[192:193], v171 offset:8192
	v_mfma_f32_32x32x16_bf16 v[114:129], v[172:175], v[188:191], v[114:129]
	s_waitcnt lgkmcnt(0)
	v_cvt_pk_f32_fp8_e32 v[194:195], v192
	v_cvt_pk_f32_fp8_e32 v[196:197], v193
	v_mfma_f32_32x32x16_bf16 v[18:33], v[176:179], v[188:191], v[18:33]
	v_mfma_f32_32x32x16_bf16 v[66:81], v[180:183], v[188:191], v[66:81]
	v_mfma_f32_32x32x16_bf16 v[2:17], v[184:187], v[188:191], v[2:17]
	v_cvt_pk_f32_fp8_sdwa v[190:191], v192 src0_sel:WORD_1
	v_cvt_pk_f32_fp8_sdwa v[192:193], v193 src0_sel:WORD_1
	v_cvt_pk_bf16_f32 v188, v194, v195
	v_cvt_pk_bf16_f32 v189, v190, v191
	v_cvt_pk_bf16_f32 v190, v196, v197
	v_cvt_pk_bf16_f32 v191, v192, v193
	s_nop 0
	v_mfma_f32_32x32x16_bf16 v[82:97], v[172:175], v[188:191], v[82:97]
	v_mfma_f32_32x32x16_bf16 v[50:65], v[176:179], v[188:191], v[50:65]
	v_mfma_f32_32x32x16_bf16 v[98:113], v[180:183], v[188:191], v[98:113]
	v_mfma_f32_32x32x16_bf16 v[34:49], v[184:187], v[188:191], v[34:49]
	s_add_u32 s56, s14, s10
	s_waitcnt vmcnt(6)
	s_addc_u32 s57, s15, 0
	s_mov_b32 m0, s54
	s_waitcnt lgkmcnt(0)
	s_barrier
	v_lshl_add_u64 v[172:173], s[56:57], 0, v[146:147]
	global_load_lds_dwordx4 v[172:173], off
	v_lshl_add_u64 v[172:173], s[56:57], 0, v[158:159]
	s_add_i32 m0, s54, 0x2000
	s_addk_i32 s53, 0x402
	global_load_lds_dwordx4 v[172:173], off
	s_bfe_u32 s10, s53, 0x70009
	s_mul_i32 s10, s10, 3
	s_sub_i32 s10, s37, s10
	s_add_i32 s10, s10, 6
	s_and_b32 s10, s10, 0xff
	s_lshl_b32 s10, s10, 14
	s_add_i32 s37, s39, s10
	s_waitcnt vmcnt(6)
	s_cmp_lt_u32 s52, 60
	v_cvt_pk_bf16_f32 v138, v138, v142
	ds_write_b32 v169, v138 offset:49152
	v_cvt_pk_bf16_f32 v138, v139, v143
	s_cselect_b32 s10, s36, 0x7e0
	ds_write_b32 v169, v138 offset:49216
	v_cvt_pk_bf16_f32 v138, v140, v144
	s_lshl_b64 s[54:55], s[10:11], 11
	ds_write_b32 v169, v138 offset:49280
	v_cvt_pk_bf16_f32 v138, v141, v145
	ds_write_b32 v169, v138 offset:49344
	v_lshl_add_u64 v[142:143], v[156:157], 0, s[54:55]
	global_load_dwordx4 v[138:141], v[142:143], off sc1 nt
	v_lshl_add_u64 v[142:143], v[142:143], 0, s[22:23]
	global_load_dwordx4 v[142:145], v[142:143], off sc1 nt
	v_add_u32_e32 v171, s37, v160
	v_add_u32_e32 v198, v171, v163
	ds_read_b64 v[188:189], v198
	ds_read_b128 v[172:175], v154 offset:57344
	ds_read_b128 v[176:179], v154 offset:59392
	ds_read_b128 v[180:183], v154 offset:61440
	ds_read_b128 v[184:187], v154 offset:63488
	s_waitcnt lgkmcnt(0)
	v_cvt_pk_f32_fp8_e32 v[190:191], v188
	v_cvt_pk_f32_fp8_sdwa v[192:193], v188 src0_sel:WORD_1
	v_cvt_pk_f32_fp8_e32 v[194:195], v189
	v_cvt_pk_f32_fp8_sdwa v[196:197], v189 src0_sel:WORD_1
	v_cvt_pk_bf16_f32 v188, v190, v191
	v_cvt_pk_bf16_f32 v189, v192, v193
	v_cvt_pk_bf16_f32 v190, v194, v195
	v_cvt_pk_bf16_f32 v191, v196, v197
	ds_read_b64 v[192:193], v198 offset:8192
	s_waitcnt lgkmcnt(0)
	v_cvt_pk_f32_fp8_e32 v[194:195], v192
	v_cvt_pk_f32_fp8_sdwa v[196:197], v192 src0_sel:WORD_1
	v_cvt_pk_f32_fp8_e32 v[198:199], v193
	v_cvt_pk_f32_fp8_sdwa v[200:201], v193 src0_sel:WORD_1
	v_cvt_pk_bf16_f32 v192, v194, v195
	v_cvt_pk_bf16_f32 v193, v196, v197
	v_cvt_pk_bf16_f32 v194, v198, v199
	v_cvt_pk_bf16_f32 v195, v200, v201
	s_nop 1
	v_mfma_f32_32x32x16_bf16 v[114:129], v[172:175], v[188:191], v[114:129]
	v_mfma_f32_32x32x16_bf16 v[18:33], v[176:179], v[188:191], v[18:33]
	v_mfma_f32_32x32x16_bf16 v[66:81], v[180:183], v[188:191], v[66:81]
	v_mfma_f32_32x32x16_bf16 v[2:17], v[184:187], v[188:191], v[2:17]
	v_mfma_f32_32x32x16_bf16 v[82:97], v[172:175], v[192:195], v[82:97]
	v_mfma_f32_32x32x16_bf16 v[50:65], v[176:179], v[192:195], v[50:65]
	v_mfma_f32_32x32x16_bf16 v[98:113], v[180:183], v[192:195], v[98:113]
	v_mfma_f32_32x32x16_bf16 v[34:49], v[184:187], v[192:195], v[34:49]
	v_add_u32_e32 v154, v171, v165
	ds_read_b64 v[188:189], v154
	ds_read_b128 v[172:175], v202 offset:57344
	ds_read_b128 v[176:179], v202 offset:59392
	ds_read_b128 v[180:183], v202 offset:61440
	ds_read_b128 v[184:187], v202 offset:63488
	s_waitcnt lgkmcnt(0)
	v_cvt_pk_f32_fp8_e32 v[190:191], v188
	v_cvt_pk_f32_fp8_sdwa v[192:193], v188 src0_sel:WORD_1
	v_cvt_pk_f32_fp8_e32 v[194:195], v189
	v_cvt_pk_f32_fp8_sdwa v[196:197], v189 src0_sel:WORD_1
	v_cvt_pk_bf16_f32 v188, v190, v191
	v_cvt_pk_bf16_f32 v189, v192, v193
	v_cvt_pk_bf16_f32 v190, v194, v195
	v_cvt_pk_bf16_f32 v191, v196, v197
	ds_read_b64 v[192:193], v154 offset:8192
	v_mfma_f32_32x32x16_bf16 v[114:129], v[172:175], v[188:191], v[114:129]
	s_waitcnt lgkmcnt(0)
	v_cvt_pk_f32_fp8_e32 v[194:195], v192
	v_cvt_pk_f32_fp8_e32 v[196:197], v193
	v_mfma_f32_32x32x16_bf16 v[18:33], v[176:179], v[188:191], v[18:33]
	v_mfma_f32_32x32x16_bf16 v[66:81], v[180:183], v[188:191], v[66:81]
	v_mfma_f32_32x32x16_bf16 v[2:17], v[184:187], v[188:191], v[2:17]
	v_cvt_pk_f32_fp8_sdwa v[190:191], v192 src0_sel:WORD_1
	v_cvt_pk_f32_fp8_sdwa v[192:193], v193 src0_sel:WORD_1
	v_cvt_pk_bf16_f32 v188, v194, v195
	v_cvt_pk_bf16_f32 v189, v190, v191
	v_cvt_pk_bf16_f32 v190, v196, v197
	v_cvt_pk_bf16_f32 v191, v192, v193
	s_nop 0
	v_mfma_f32_32x32x16_bf16 v[82:97], v[172:175], v[188:191], v[82:97]
	v_mfma_f32_32x32x16_bf16 v[50:65], v[176:179], v[188:191], v[50:65]
	v_mfma_f32_32x32x16_bf16 v[98:113], v[180:183], v[188:191], v[98:113]
	v_mfma_f32_32x32x16_bf16 v[34:49], v[184:187], v[188:191], v[34:49]
	s_add_u32 s54, s14, s10
	s_waitcnt vmcnt(6)
	s_addc_u32 s55, s15, 0
	s_mov_b32 m0, s37
	s_waitcnt lgkmcnt(0)
	s_barrier
	v_lshl_add_u64 v[172:173], s[54:55], 0, v[146:147]
	global_load_lds_dwordx4 v[172:173], off
	v_lshl_add_u64 v[172:173], s[54:55], 0, v[158:159]
	s_add_i32 m0, s37, 0x2000
	s_add_i32 s36, s36, 64
	global_load_lds_dwordx4 v[172:173], off
	s_cmp_gt_u32 s52, 61
	s_mov_b32 s37, s52
	s_cbranch_scc0 .Lmoe_B_1019
.Lmoe_X_1019:
	s_waitcnt vmcnt(0)
.LBB0_1021:
	s_waitcnt vmcnt(0)
	s_add_i32 s51, s51, s49
	v_cmp_gt_i32_e32 vcc, s50, v166
	s_and_saveexec_b64 s[36:37], vcc
	s_cbranch_execz .LBB0_1023
	v_mov_b32_e32 v130, s48
	ds_read_b32 v130, v130 offset:32
	v_add_u32_e32 v131, s49, v166
	v_mul_f32_e32 v136, 0xbfb8aa3b, v114
	v_mul_f32_e32 v137, 0xbfb8aa3b, v115
	v_mul_f32_e32 v138, 0xbfb8aa3b, v116
	s_waitcnt lgkmcnt(0)
	v_cmp_gt_i32_e32 vcc, v130, v131
	v_mov_b32_e32 v134, v68
	v_mul_f32_e32 v68, 0xbfb8aa3b, v117
	v_cndmask_b32_e64 v130, 8, 0, vcc
	v_lshl_add_u32 v132, v130, 2, s48
	ds_read_b32 v132, v132 offset:16
	v_or_b32_e32 v133, 4, v130
	v_mul_f32_e32 v139, 0xbfb8aa3b, v118
	v_mul_f32_e32 v140, 0xbfb8aa3b, v119
	v_mul_f32_e32 v141, 0xbfb8aa3b, v120
	s_waitcnt lgkmcnt(0)
	v_cmp_gt_i32_e32 vcc, v132, v131
	v_mul_f32_e32 v142, 0xbfb8aa3b, v121
	v_mul_f32_e32 v143, 0xbfb8aa3b, v122
	v_cndmask_b32_e32 v130, v133, v130, vcc
	v_lshl_add_u32 v132, v130, 2, s48
	ds_read_b32 v132, v132 offset:8
	v_or_b32_e32 v133, 2, v130
	v_mul_f32_e32 v144, 0xbfb8aa3b, v123
	v_exp_f32_e32 v136, v136
	v_exp_f32_e32 v137, v137
	s_waitcnt lgkmcnt(0)
	v_cmp_gt_i32_e32 vcc, v132, v131
	v_exp_f32_e32 v138, v138
	v_exp_f32_e32 v68, v68
	v_cndmask_b32_e32 v130, v133, v130, vcc
	v_lshl_add_u32 v132, v130, 2, s48
	ds_read_b32 v132, v132 offset:4
	v_or_b32_e32 v133, 1, v130
	v_exp_f32_e32 v139, v139
	v_exp_f32_e32 v140, v140
	v_exp_f32_e32 v141, v141
	s_waitcnt lgkmcnt(0)
	v_cmp_gt_i32_e32 vcc, v132, v131
	v_add_u32_e32 v131, s47, v131
	v_exp_f32_e32 v142, v142
	v_cndmask_b32_e32 v130, v133, v130, vcc
	v_lshl_add_u32 v132, v130, 2, s48
	ds_read_b32 v132, v132
	v_exp_f32_e32 v143, v143
	v_exp_f32_e32 v144, v144
	v_add_f32_e32 v136, 1.0, v136
	v_add_f32_e32 v137, 1.0, v137
	s_waitcnt lgkmcnt(0)
	v_sub_u32_e32 v131, v131, v132
	v_lshl_add_u32 v130, v130, 9, v131
	v_ashrrev_i32_e32 v131, 31, v130
	v_lshl_add_u64 v[130:131], v[130:131], 2, s[8:9]
	global_load_dword v135, v[130:131], off
	v_add_f32_e32 v138, 1.0, v138
	v_add_f32_e32 v68, 1.0, v68
	v_add_f32_e32 v139, 1.0, v139
	v_add_f32_e32 v140, 1.0, v140
	v_add_f32_e32 v141, 1.0, v141
	v_add_f32_e32 v142, 1.0, v142
	v_add_f32_e32 v143, 1.0, v143
	v_add_f32_e32 v144, 1.0, v144
	v_rcp_f32_e32 v136, v136
	v_rcp_f32_e32 v137, v137
	v_rcp_f32_e32 v138, v138
	v_rcp_f32_e32 v68, v68
	v_rcp_f32_e32 v139, v139
	v_rcp_f32_e32 v140, v140
	v_rcp_f32_e32 v141, v141
	v_rcp_f32_e32 v142, v142
	v_rcp_f32_e32 v143, v143
	v_rcp_f32_e32 v144, v144
	v_mul_f32_e32 v114, v114, v136
	v_mul_f32_e32 v115, v115, v137
	v_mul_f32_e32 v154, v116, v138
	v_mul_f32_e32 v68, v117, v68
	v_mul_f32_e32 v116, v118, v139
	v_mul_f32_e32 v117, v119, v140
	v_mul_f32_e32 v118, v120, v141
	v_mul_f32_e32 v119, v121, v142
	v_mul_f32_e32 v120, v122, v143
	v_mul_f32_e32 v121, v123, v144
	v_mul_f32_e32 v114, v66, v114
	v_mul_f32_e32 v115, v67, v115
	v_mul_f32_e32 v145, 0xbfb8aa3b, v124
	v_mul_f32_e32 v146, 0xbfb8aa3b, v125
	v_mul_f32_e32 v68, v69, v68
	v_mul_f32_e32 v69, v70, v116
	v_mul_f32_e32 v70, v71, v117
	v_mul_f32_e32 v71, v72, v118
	v_mul_f32_e32 v72, v73, v119
	v_mul_f32_e32 v73, v74, v120
	v_mul_f32_e32 v74, v75, v121
	v_mov_b32_e32 v132, v147
	v_exp_f32_e32 v145, v145
	v_exp_f32_e32 v146, v146
	v_mov_b32_e32 v133, v147
	v_add_u32_e32 v130, s51, v166
	v_add_f32_e32 v145, 1.0, v145
	v_add_f32_e32 v146, 1.0, v146
	v_rcp_f32_e32 v145, v145
	v_ashrrev_i32_e32 v131, 31, v130
	v_lshlrev_b64 v[130:131], 9, v[130:131]
	v_lshl_add_u64 v[130:131], s[20:21], 0, v[130:131]
	v_lshl_add_u64 v[130:131], v[130:131], 0, s[34:35]
	v_lshl_add_u64 v[130:131], v[130:131], 0, v[150:151]
	s_waitcnt vmcnt(0)
	v_pk_mul_f32 v[66:67], v[134:135], v[154:155]
	s_nop 0
	v_mul_f32_e32 v75, v114, v67
	v_mul_f32_e32 v114, v115, v67
	v_med3_f32 v75, v75, s45, v170
	v_med3_f32 v114, v114, s45, v170
	v_mul_f32_e32 v69, v69, v67
	v_mul_f32_e32 v70, v70, v67
	v_cvt_pk_fp8_f32 v132, v75, v114
	v_mul_f32_e32 v71, v71, v67
	v_med3_f32 v69, v69, s45, v170
	v_med3_f32 v70, v70, s45, v170
	v_mul_f32_e32 v66, v66, v67
	v_mul_f32_e32 v68, v68, v67
	v_cvt_pk_fp8_f32 v133, v69, v70
	v_med3_f32 v69, v71, s45, v170
	v_mul_f32_e32 v71, 0xbfb8aa3b, v126
	v_med3_f32 v66, v66, s45, v170
	v_med3_f32 v68, v68, s45, v170
	v_exp_f32_e32 v71, v71
	v_mul_f32_e32 v72, v72, v67
	v_cvt_pk_fp8_f32 v132, v66, v68 op_sel:[0,0,1]
	v_rcp_f32_e32 v66, v146
	v_mul_f32_e32 v73, v73, v67
	v_mul_f32_e32 v74, v74, v67
	v_med3_f32 v70, v72, s45, v170
	v_cvt_pk_fp8_f32 v133, v69, v70 op_sel:[0,0,1]
	v_med3_f32 v69, v73, s45, v170
	v_med3_f32 v70, v74, s45, v170
	v_mov_b32_e32 v134, v147
	v_cvt_pk_fp8_f32 v134, v69, v70
	v_mul_f32_e32 v69, 0xbfb8aa3b, v127
	v_add_f32_e32 v70, 1.0, v71
	v_mul_f32_e32 v68, v124, v145
	v_mul_f32_e32 v66, v125, v66
	v_exp_f32_e32 v69, v69
	v_rcp_f32_e32 v70, v70
	v_mul_f32_e32 v68, v76, v68
	v_mul_f32_e32 v66, v77, v66
	v_mul_f32_e32 v68, v68, v67
	v_mul_f32_e32 v66, v66, v67
	v_med3_f32 v68, v68, s45, v170
	v_med3_f32 v66, v66, s45, v170
	v_cvt_pk_fp8_f32 v134, v68, v66 op_sel:[0,0,1]
	v_add_f32_e32 v66, 1.0, v69
	v_mul_f32_e32 v68, v126, v70
	v_mul_f32_e32 v69, 0xbfb8aa3b, v128
	v_mul_f32_e32 v70, 0xbfb8aa3b, v129
	v_exp_f32_e32 v69, v69
	v_exp_f32_e32 v70, v70
	v_rcp_f32_e32 v66, v66
	v_mul_f32_e32 v68, v78, v68
	v_add_f32_e32 v69, 1.0, v69
	v_add_f32_e32 v70, 1.0, v70
	v_mul_f32_e32 v66, v127, v66
	v_rcp_f32_e32 v69, v69
	v_rcp_f32_e32 v70, v70
	v_mul_f32_e32 v66, v79, v66
	v_mul_f32_e32 v68, v68, v67
	v_mul_f32_e32 v66, v66, v67
	v_med3_f32 v68, v68, s45, v170
	v_med3_f32 v66, v66, s45, v170
	v_mov_b32_e32 v135, v147
	v_mul_f32_e32 v69, v128, v69
	v_mul_f32_e32 v70, v129, v70
	v_cvt_pk_fp8_f32 v135, v68, v66
	v_mul_f32_e32 v69, v80, v69
	v_mul_f32_e32 v70, v81, v70
	v_mul_f32_e32 v69, v69, v67
	v_mul_f32_e32 v66, v70, v67
	v_med3_f32 v68, v69, s45, v170
	v_med3_f32 v66, v66, s45, v170
	v_cvt_pk_fp8_f32 v135, v68, v66 op_sel:[0,0,1]
	v_mul_f32_e32 v66, 0xbfb8aa3b, v18
	v_exp_f32_e32 v66, v66
	v_mul_f32_e32 v68, 0xbfb8aa3b, v19
	v_exp_f32_e32 v68, v68
	v_permlane32_swap_b32_e32 v132, v133
	v_add_f32_e32 v66, 1.0, v66
	v_rcp_f32_e32 v66, v66
	v_add_f32_e32 v68, 1.0, v68
	v_rcp_f32_e32 v68, v68
	v_permlane32_swap_b32_e32 v134, v135
	v_mul_f32_e32 v18, v18, v66
	v_mul_f32_e32 v2, v2, v18
	v_mul_f32_e32 v18, v19, v68
	v_mul_f32_e32 v3, v3, v18
	v_mul_f32_e32 v18, 0xbfb8aa3b, v21
	v_mul_f32_e32 v19, 0xbfb8aa3b, v20
	v_exp_f32_e32 v18, v18
	v_exp_f32_e32 v19, v19
	v_mul_f32_e32 v2, v2, v67
	v_mul_f32_e32 v3, v3, v67
	v_add_f32_e32 v18, 1.0, v18
	v_add_f32_e32 v19, 1.0, v19
	v_rcp_f32_e32 v18, v18
	v_rcp_f32_e32 v19, v19
	v_med3_f32 v3, v3, s45, v170
	v_permlane32_swap_b32_e32 v132, v134
	v_mul_f32_e32 v18, v21, v18
	v_mul_f32_e32 v19, v20, v19
	v_mul_f32_e32 v5, v5, v18
	v_med3_f32 v18, v2, s45, v170
	v_mov_b32_e32 v2, v147
	v_mul_f32_e32 v4, v4, v19
	v_mul_f32_e32 v19, 0xbfb8aa3b, v22
	v_cvt_pk_fp8_f32 v2, v18, v3
	v_exp_f32_e32 v19, v19
	v_mul_f32_e32 v4, v4, v67
	v_mul_f32_e32 v5, v5, v67
	v_med3_f32 v4, v4, s45, v170
	v_med3_f32 v5, v5, s45, v170
	v_cvt_pk_fp8_f32 v2, v4, v5 op_sel:[0,0,1]
	v_mul_f32_e32 v5, 0xbfb8aa3b, v24
	v_add_f32_e32 v18, 1.0, v19
	v_exp_f32_e32 v5, v5
	v_mul_f32_e32 v3, 0xbfb8aa3b, v23
	v_rcp_f32_e32 v18, v18
	v_exp_f32_e32 v3, v3
	v_add_f32_e32 v5, 1.0, v5
	v_rcp_f32_e32 v5, v5
	v_mul_f32_e32 v4, v22, v18
	v_add_f32_e32 v3, 1.0, v3
	v_mul_f32_e32 v4, v6, v4
	v_mul_f32_e32 v6, 0xbfb8aa3b, v25
	v_rcp_f32_e32 v3, v3
	v_exp_f32_e32 v6, v6
	v_mul_f32_e32 v5, v24, v5
	v_mul_f32_e32 v5, v8, v5
	v_mul_f32_e32 v8, 0xbfb8aa3b, v26
	v_mul_f32_e32 v3, v23, v3
	v_add_f32_e32 v6, 1.0, v6
	v_exp_f32_e32 v8, v8
	v_mul_f32_e32 v3, v7, v3
	v_rcp_f32_e32 v6, v6
	v_mul_f32_e32 v4, v4, v67
	v_mul_f32_e32 v3, v3, v67
	v_med3_f32 v4, v4, s45, v170
	v_med3_f32 v7, v3, s45, v170
	v_mov_b32_e32 v3, v147
	v_cvt_pk_fp8_f32 v3, v4, v7
	v_mul_f32_e32 v4, 0xbfb8aa3b, v27
	v_add_f32_e32 v7, 1.0, v8
	v_mul_f32_e32 v6, v25, v6
	v_exp_f32_e32 v4, v4
	v_rcp_f32_e32 v7, v7
	v_mul_f32_e32 v6, v9, v6
	v_mul_f32_e32 v5, v5, v67
	v_mul_f32_e32 v6, v6, v67
	v_med3_f32 v5, v5, s45, v170
	v_med3_f32 v6, v6, s45, v170
	v_cvt_pk_fp8_f32 v3, v5, v6 op_sel:[0,0,1]
	v_add_f32_e32 v4, 1.0, v4
	v_mul_f32_e32 v5, v26, v7
	v_mul_f32_e32 v6, 0xbfb8aa3b, v28
	v_mul_f32_e32 v7, 0xbfb8aa3b, v29
	v_rcp_f32_e32 v4, v4
	v_exp_f32_e32 v6, v6
	v_exp_f32_e32 v7, v7
	v_mul_f32_e32 v9, 0xbfb8aa3b, v30
	v_mul_f32_e32 v4, v27, v4
	v_add_f32_e32 v6, 1.0, v6
	v_add_f32_e32 v7, 1.0, v7
	v_exp_f32_e32 v9, v9
	v_mul_f32_e32 v5, v10, v5
	v_mul_f32_e32 v4, v11, v4
	v_rcp_f32_e32 v6, v6
	v_rcp_f32_e32 v7, v7
	v_mul_f32_e32 v5, v5, v67
	v_mul_f32_e32 v4, v4, v67
	v_med3_f32 v5, v5, s45, v170
	v_med3_f32 v8, v4, s45, v170
	v_mov_b32_e32 v4, v147
	v_cvt_pk_fp8_f32 v4, v5, v8
	v_add_f32_e32 v8, 1.0, v9
	v_mul_f32_e32 v6, v28, v6
	v_mul_f32_e32 v7, v29, v7
	v_mul_f32_e32 v5, 0xbfb8aa3b, v31
	v_rcp_f32_e32 v8, v8
	v_mul_f32_e32 v6, v12, v6
	v_mul_f32_e32 v7, v13, v7
	v_exp_f32_e32 v5, v5
	v_mul_f32_e32 v6, v6, v67
	v_mul_f32_e32 v7, v7, v67
	v_med3_f32 v6, v6, s45, v170
	v_med3_f32 v7, v7, s45, v170
	v_cvt_pk_fp8_f32 v4, v6, v7 op_sel:[0,0,1]
	v_mul_f32_e32 v6, v30, v8
	v_mul_f32_e32 v7, 0xbfb8aa3b, v32
	v_mul_f32_e32 v8, 0xbfb8aa3b, v33
	v_add_f32_e32 v5, 1.0, v5
	v_exp_f32_e32 v7, v7
	v_exp_f32_e32 v8, v8
	v_rcp_f32_e32 v5, v5
	v_mul_f32_e32 v6, v14, v6
	v_add_f32_e32 v7, 1.0, v7
	v_add_f32_e32 v8, 1.0, v8
	v_mul_f32_e32 v5, v31, v5
	v_rcp_f32_e32 v7, v7
	v_rcp_f32_e32 v8, v8
	v_mul_f32_e32 v5, v15, v5
	v_mul_f32_e32 v6, v6, v67
	v_mul_f32_e32 v5, v5, v67
	v_med3_f32 v6, v6, s45, v170
	v_med3_f32 v9, v5, s45, v170
	v_mov_b32_e32 v5, v147
	v_mul_f32_e32 v7, v32, v7
	v_mul_f32_e32 v8, v33, v8
	v_cvt_pk_fp8_f32 v5, v6, v9
	v_mul_f32_e32 v7, v16, v7
	v_mul_f32_e32 v8, v17, v8
	v_mul_f32_e32 v7, v7, v67
	v_mul_f32_e32 v6, v8, v67
	v_med3_f32 v7, v7, s45, v170
	v_med3_f32 v6, v6, s45, v170
	v_cvt_pk_fp8_f32 v5, v7, v6 op_sel:[0,0,1]
	v_permlane32_swap_b32_e32 v2, v3
	v_permlane32_swap_b32_e32 v133, v135
	v_permlane32_swap_b32_e32 v4, v5
	s_nop 1
	v_permlane32_swap_b32_e32 v2, v4
	v_permlane32_swap_b32_e32 v3, v5
	global_store_dwordx4 v[130:131], v[132:135], off
	global_store_dwordx4 v[130:131], v[2:5], off offset:32

.LBB0_1084:
	s_add_i32 s31, s30, s34
	s_lshl_b32 s35, s31, 2
	s_add_i32 s35, s35, 0
	s_add_i32 s35, s35, 0x20000
	v_mov_b32_e32 v2, s35
	ds_read_b32 v2, v2
	s_waitcnt lgkmcnt(0)
	v_readfirstlane_b32 s35, v2
	s_cmp_gt_i32 s35, s10
	s_cselect_b32 s34, s34, s31
	s_lshr_b32 s31, s30, 1
	s_cmp_lt_u32 s30, 2
	s_mov_b32 s30, s31
	s_cbranch_scc0 .LBB0_1084
	s_lshl_b32 s30, s34, 2
	s_add_i32 s30, s30, 0
	s_add_i32 s30, s30, 0x20000
	v_mov_b32_e32 v4, s30
	ds_read2_b32 v[2:3], v4 offset1:80
	ds_read_b32 v4, v4 offset:640
	s_mov_b32 s35, s11
	s_waitcnt lgkmcnt(1)
	v_readfirstlane_b32 s30, v2
	s_sub_i32 s30, s10, s30
	v_readfirstlane_b32 s31, v3
	s_lshl_b32 s47, s30, 9
	s_waitcnt lgkmcnt(0)
	v_readfirstlane_b32 s49, v4
	s_sub_i32 s30, s31, s47
	s_add_i32 s49, s49, s47
	s_min_i32 s48, s30, 0x200
	s_lshl_b64 s[30:31], s[34:35], 22
	s_add_u32 s35, s6, s30
	s_addc_u32 s50, s7, s31
	s_lshl_b32 s10, s10, 11
	s_lshl_b32 s30, s46, 7
	s_sub_i32 s30, s30, s10
	s_ashr_i32 s31, s30, 31
	v_cmp_gt_i32_e32 vcc, s48, v0
	s_lshl_b64 s[36:37], s[30:31], 2
	s_add_u32 s36, s35, s36
	v_cndmask_b32_e32 v2, 0, v0, vcc
	v_add_u32_e32 v2, s49, v2
	s_addc_u32 s37, s50, s37
	v_lshl_or_b32 v146, v2, 9, v1
	v_lshl_add_u64 v[2:3], s[36:37], 0, v[152:153]
	v_lshl_add_u64 v[154:155], v[2:3], 0, v[148:149]
	s_mov_b64 s[36:37], -1
	s_cmp_ge_i32 s38, s48
	v_lshl_add_u64 v[132:133], v[154:155], 0, s[20:21]
	v_lshl_add_u64 v[130:131], v[154:155], 0, s[22:23]
	v_lshl_add_u64 v[134:135], v[154:155], 0, s[24:25]
	v_lshl_add_u64 v[138:139], v[154:155], 0, s[26:27]
	v_lshl_add_u64 v[142:143], v[154:155], 0, s[28:29]
	s_cbranch_scc0 .LBB0_1089
	global_load_dwordx4 v[2:5], v[154:155], off sc1 nt
	s_mov_b32 m0, s39
	global_load_dwordx4 v[6:9], v[132:133], off sc1 nt
	v_lshl_add_u64 v[82:83], s[12:13], 0, v[146:147]
	global_load_lds_dwordx4 v146, s[12:13]
	global_load_dwordx4 v[66:69], v[130:131], off sc1 nt
	global_load_dwordx4 v[70:73], v[134:135], off sc1 nt
	s_mov_b32 m0, s40
	s_nop 0
	global_load_lds_dwordx4 v146, s[14:15]
	s_waitcnt vmcnt(4)
	s_nop 0
	v_cvt_pk_bf16_f32 v2, v2, v6
	ds_write_b32 v167, v2 offset:49152
	v_cvt_pk_bf16_f32 v2, v3, v7
	ds_write_b32 v167, v2 offset:49216
	v_cvt_pk_bf16_f32 v2, v4, v8
	ds_write_b32 v167, v2 offset:49280
	v_cvt_pk_bf16_f32 v2, v5, v9
	ds_write_b32 v167, v2 offset:49344
	global_load_dwordx4 v[74:77], v[138:139], off sc1 nt
	global_load_dwordx4 v[78:81], v[142:143], off sc1 nt
	s_waitcnt vmcnt(5)
	s_mov_b32 m0, s41
	s_waitcnt lgkmcnt(0)
	s_barrier
	global_load_lds_dwordx4 v146, s[16:17]
	v_mov_b32_e32 v2, 0
	s_mov_b32 s36, -2
	s_movk_i32 s35, 0x80
	v_mov_b32_e32 v3, v2
	v_mov_b32_e32 v4, v2
	v_mov_b32_e32 v5, v2
	v_mov_b32_e32 v6, v2
	v_mov_b32_e32 v7, v2
	v_mov_b32_e32 v8, v2
	v_mov_b32_e32 v9, v2
	v_mov_b32_e32 v10, v2
	v_mov_b32_e32 v11, v2
	v_mov_b32_e32 v12, v2
	v_mov_b32_e32 v13, v2
	v_mov_b32_e32 v14, v2
	v_mov_b32_e32 v15, v2
	v_mov_b32_e32 v16, v2
	v_mov_b32_e32 v17, v2
	v_mov_b32_e32 v18, v2
	v_mov_b32_e32 v19, v2
	v_mov_b32_e32 v20, v2
	v_mov_b32_e32 v21, v2
	v_mov_b32_e32 v22, v2
	v_mov_b32_e32 v23, v2
	v_mov_b32_e32 v24, v2
	v_mov_b32_e32 v25, v2
	v_mov_b32_e32 v26, v2
	v_mov_b32_e32 v27, v2
	v_mov_b32_e32 v28, v2
	v_mov_b32_e32 v29, v2
	v_mov_b32_e32 v30, v2
	v_mov_b32_e32 v31, v2
	v_mov_b32_e32 v32, v2
	v_mov_b32_e32 v33, v2
	v_mov_b32_e32 v34, v2
	v_mov_b32_e32 v35, v2
	v_mov_b32_e32 v36, v2
	v_mov_b32_e32 v37, v2
	v_mov_b32_e32 v38, v2
	v_mov_b32_e32 v39, v2
	v_mov_b32_e32 v40, v2
	v_mov_b32_e32 v41, v2
	v_mov_b32_e32 v42, v2
	v_mov_b32_e32 v43, v2
	v_mov_b32_e32 v44, v2
	v_mov_b32_e32 v45, v2
	v_mov_b32_e32 v46, v2
	v_mov_b32_e32 v47, v2
	v_mov_b32_e32 v48, v2
	v_mov_b32_e32 v49, v2
	v_mov_b32_e32 v50, v2
	v_mov_b32_e32 v51, v2
	v_mov_b32_e32 v52, v2
	v_mov_b32_e32 v53, v2
	v_mov_b32_e32 v54, v2
	v_mov_b32_e32 v55, v2
	v_mov_b32_e32 v56, v2
	v_mov_b32_e32 v57, v2
	v_mov_b32_e32 v58, v2
	v_mov_b32_e32 v59, v2
	v_mov_b32_e32 v60, v2
	v_mov_b32_e32 v61, v2
	v_mov_b32_e32 v62, v2
	v_mov_b32_e32 v63, v2
	v_mov_b32_e32 v64, v2
	v_mov_b32_e32 v65, v2
	v_readfirstlane_b32 s98, v250
	s_bitcmp1_b32 s98, 8
	s_cbranch_scc1 .Lmoe_B_1087
.LBB0_1087:
	s_mul_i32 s52, s36, 0xab
	s_add_i32 s10, s52, 0x357
	s_bfe_u32 s10, s10, 0x70009
	s_mul_i32 s10, s10, 3
	s_sub_i32 s10, s36, s10
	s_add_i32 s10, s10, 5
	s_and_b32 s10, s10, 0xff
	s_lshl_b32 s10, s10, 14
	s_add_i32 s53, s39, s10
	s_add_i32 s37, s36, 2
	v_add_u32_e32 v111, s53, v158
	v_add_u32_e32 v84, v111, v161
	v_add_u32_e32 v110, v159, v160
	ds_read_b64 v[100:101], v84
	ds_read_b128 v[84:87], v110 offset:49152
	ds_read_b128 v[88:91], v110 offset:51200
	ds_read_b128 v[92:95], v110 offset:53248
	ds_read_b128 v[96:99], v110 offset:55296
	s_waitcnt lgkmcnt(0)
	v_cvt_pk_f32_fp8_e32 v[102:103], v100
	v_cvt_pk_f32_fp8_sdwa v[104:105], v100 src0_sel:WORD_1
	v_cvt_pk_f32_fp8_e32 v[106:107], v101
	v_cvt_pk_f32_fp8_sdwa v[108:109], v101 src0_sel:WORD_1
	v_cvt_pk_bf16_f32 v100, v102, v103
	v_cvt_pk_bf16_f32 v101, v104, v105
	v_cvt_pk_bf16_f32 v102, v106, v107
	v_cvt_pk_bf16_f32 v103, v108, v109
	s_waitcnt vmcnt(4)
	s_sub_i32 s10, s35, 32
	v_cvt_pk_bf16_f32 v66, v66, v70
	s_cmp_lt_u32 s37, 13
	ds_write_b32 v167, v66 offset:57344
	v_cvt_pk_bf16_f32 v66, v67, v71
	s_cselect_b32 s10, s10, 0x1e0
	ds_write_b32 v167, v66 offset:57408
	v_cvt_pk_bf16_f32 v66, v68, v72
	s_lshl_b64 s[50:51], s[10:11], 13
	ds_write_b32 v167, v66 offset:57472
	v_cvt_pk_bf16_f32 v66, v69, v73
	ds_write_b32 v167, v66 offset:57536
	v_lshl_add_u64 v[70:71], v[154:155], 0, s[50:51]
	global_load_dwordx4 v[66:69], v[70:71], off sc1 nt
	v_lshl_add_u64 v[70:71], v[70:71], 0, s[20:21]
	global_load_dwordx4 v[70:73], v[70:71], off sc1 nt
	v_mfma_f32_32x32x16_bf16 v[50:65], v[84:87], v[100:103], v[50:65]
	v_mfma_f32_32x32x16_bf16 v[34:49], v[88:91], v[100:103], v[34:49]
	v_mfma_f32_32x32x16_bf16 v[18:33], v[92:95], v[100:103], v[18:33]
	v_mfma_f32_32x32x16_bf16 v[2:17], v[96:99], v[100:103], v[2:17]
	v_add_u32_e32 v84, v111, v163
	v_add_u32_e32 v112, v159, v162
	ds_read_b64 v[100:101], v84
	ds_read_b128 v[84:87], v112 offset:49152
	ds_read_b128 v[88:91], v112 offset:51200
	ds_read_b128 v[92:95], v112 offset:53248
	ds_read_b128 v[96:99], v112 offset:55296
	s_waitcnt lgkmcnt(0)
	v_cvt_pk_f32_fp8_e32 v[102:103], v100
	v_cvt_pk_f32_fp8_sdwa v[104:105], v100 src0_sel:WORD_1
	v_cvt_pk_f32_fp8_e32 v[106:107], v101
	v_cvt_pk_f32_fp8_sdwa v[108:109], v101 src0_sel:WORD_1
	v_cvt_pk_bf16_f32 v100, v102, v103
	v_cvt_pk_bf16_f32 v101, v104, v105
	v_cvt_pk_bf16_f32 v102, v106, v107
	v_cvt_pk_bf16_f32 v103, v108, v109
	s_nop 0
	v_mfma_f32_32x32x16_bf16 v[50:65], v[84:87], v[100:103], v[50:65]
	v_mfma_f32_32x32x16_bf16 v[34:49], v[88:91], v[100:103], v[34:49]
	v_mfma_f32_32x32x16_bf16 v[18:33], v[92:95], v[100:103], v[18:33]
	v_mfma_f32_32x32x16_bf16 v[2:17], v[96:99], v[100:103], v[2:17]
	s_waitcnt vmcnt(5)
	s_mov_b32 m0, s53
	s_waitcnt lgkmcnt(0)
	s_barrier
	v_lshl_add_u64 v[84:85], v[82:83], 0, s[10:11]
	global_load_lds_dwordx4 v[84:85], off
	s_addk_i32 s52, 0x402
	s_bfe_u32 s10, s52, 0x70009
	s_mul_i32 s10, s10, 3
	s_sub_i32 s10, s36, s10
	s_add_i32 s10, s10, 6
	s_and_b32 s10, s10, 0xff
	s_lshl_b32 s10, s10, 14
	s_add_i32 s36, s39, s10
	v_add_u32_e32 v111, s36, v158
	v_add_u32_e32 v84, v111, v161
	ds_read_b64 v[100:101], v84
	ds_read_b128 v[84:87], v110 offset:57344
	ds_read_b128 v[88:91], v110 offset:59392
	ds_read_b128 v[92:95], v110 offset:61440
	ds_read_b128 v[96:99], v110 offset:63488
	s_waitcnt lgkmcnt(0)
	v_cvt_pk_f32_fp8_e32 v[102:103], v100
	v_cvt_pk_f32_fp8_sdwa v[104:105], v100 src0_sel:WORD_1
	v_cvt_pk_f32_fp8_e32 v[106:107], v101
	v_cvt_pk_f32_fp8_sdwa v[108:109], v101 src0_sel:WORD_1
	v_cvt_pk_bf16_f32 v100, v102, v103
	v_cvt_pk_bf16_f32 v101, v104, v105
	v_cvt_pk_bf16_f32 v102, v106, v107
	v_cvt_pk_bf16_f32 v103, v108, v109
	s_waitcnt vmcnt(4)
	s_cmp_lt_u32 s37, 12
	v_cvt_pk_bf16_f32 v74, v74, v78
	ds_write_b32 v167, v74 offset:49152
	v_cvt_pk_bf16_f32 v74, v75, v79
	s_cselect_b32 s10, s35, 0x1e0
	ds_write_b32 v167, v74 offset:49216
	v_cvt_pk_bf16_f32 v74, v76, v80
	s_lshl_b64 s[50:51], s[10:11], 13
	ds_write_b32 v167, v74 offset:49280
	v_cvt_pk_bf16_f32 v74, v77, v81
	ds_write_b32 v167, v74 offset:49344
	v_lshl_add_u64 v[78:79], v[154:155], 0, s[50:51]
	global_load_dwordx4 v[74:77], v[78:79], off sc1 nt
	v_lshl_add_u64 v[78:79], v[78:79], 0, s[20:21]
	global_load_dwordx4 v[78:81], v[78:79], off sc1 nt
	v_mfma_f32_32x32x16_bf16 v[50:65], v[84:87], v[100:103], v[50:65]
	v_mfma_f32_32x32x16_bf16 v[34:49], v[88:91], v[100:103], v[34:49]
	v_mfma_f32_32x32x16_bf16 v[18:33], v[92:95], v[100:103], v[18:33]
	v_mfma_f32_32x32x16_bf16 v[2:17], v[96:99], v[100:103], v[2:17]
	v_add_u32_e32 v84, v111, v163
	ds_read_b64 v[100:101], v84
	ds_read_b128 v[84:87], v112 offset:57344
	ds_read_b128 v[88:91], v112 offset:59392
	ds_read_b128 v[92:95], v112 offset:61440
	ds_read_b128 v[96:99], v112 offset:63488
	s_waitcnt lgkmcnt(0)
	v_cvt_pk_f32_fp8_e32 v[102:103], v100
	v_cvt_pk_f32_fp8_sdwa v[104:105], v100 src0_sel:WORD_1
	v_cvt_pk_f32_fp8_e32 v[106:107], v101
	v_cvt_pk_f32_fp8_sdwa v[108:109], v101 src0_sel:WORD_1
	v_cvt_pk_bf16_f32 v100, v102, v103
	v_cvt_pk_bf16_f32 v101, v104, v105
	v_cvt_pk_bf16_f32 v102, v106, v107
	v_cvt_pk_bf16_f32 v103, v108, v109
	s_nop 0
	v_mfma_f32_32x32x16_bf16 v[50:65], v[84:87], v[100:103], v[50:65]
	v_mfma_f32_32x32x16_bf16 v[34:49], v[88:91], v[100:103], v[34:49]
	v_mfma_f32_32x32x16_bf16 v[18:33], v[92:95], v[100:103], v[18:33]
	v_mfma_f32_32x32x16_bf16 v[2:17], v[96:99], v[100:103], v[2:17]
	s_waitcnt vmcnt(5)
	s_mov_b32 m0, s36
	s_waitcnt lgkmcnt(0)
	s_barrier
	v_lshl_add_u64 v[84:85], v[82:83], 0, s[10:11]
	global_load_lds_dwordx4 v[84:85], off
	s_add_i32 s35, s35, 64
	s_cmp_gt_u32 s37, 13
	s_mov_b32 s36, s37
	s_cbranch_scc0 .LBB0_1087
	s_branch .Lmoe_X_1087
.Lmoe_B_1087:
	s_mul_i32 s52, s36, 0xab
	s_add_i32 s10, s52, 0x357
	s_bfe_u32 s10, s10, 0x70009
	s_mul_i32 s10, s10, 3
	s_sub_i32 s10, s36, s10
	s_add_i32 s10, s10, 5
	s_and_b32 s10, s10, 0xff
	s_lshl_b32 s10, s10, 14
	s_add_i32 s53, s39, s10
	s_add_i32 s37, s36, 2
	s_waitcnt vmcnt(4)
	s_sub_i32 s10, s35, 32
	v_cvt_pk_bf16_f32 v66, v66, v70
	s_cmp_lt_u32 s37, 13
	ds_write_b32 v167, v66 offset:57344
	v_cvt_pk_bf16_f32 v66, v67, v71
	s_cselect_b32 s10, s10, 0x1e0
	ds_write_b32 v167, v66 offset:57408
	v_cvt_pk_bf16_f32 v66, v68, v72
	s_lshl_b64 s[50:51], s[10:11], 13
	ds_write_b32 v167, v66 offset:57472
	v_cvt_pk_bf16_f32 v66, v69, v73
	ds_write_b32 v167, v66 offset:57536
	v_lshl_add_u64 v[70:71], v[154:155], 0, s[50:51]
	global_load_dwordx4 v[66:69], v[70:71], off sc1 nt
	v_lshl_add_u64 v[70:71], v[70:71], 0, s[20:21]
	global_load_dwordx4 v[70:73], v[70:71], off sc1 nt
	v_add_u32_e32 v111, s53, v158
	v_add_u32_e32 v84, v111, v161
	v_add_u32_e32 v110, v159, v160
	ds_read_b64 v[100:101], v84
	ds_read_b128 v[84:87], v110 offset:49152
	ds_read_b128 v[88:91], v110 offset:51200
	ds_read_b128 v[92:95], v110 offset:53248
	ds_read_b128 v[96:99], v110 offset:55296
	s_waitcnt lgkmcnt(0)
	v_cvt_pk_f32_fp8_e32 v[102:103], v100
	v_cvt_pk_f32_fp8_sdwa v[104:105], v100 src0_sel:WORD_1
	v_cvt_pk_f32_fp8_e32 v[106:107], v101
	v_cvt_pk_f32_fp8_sdwa v[108:109], v101 src0_sel:WORD_1
	v_cvt_pk_bf16_f32 v100, v102, v103
	v_cvt_pk_bf16_f32 v101, v104, v105
	v_cvt_pk_bf16_f32 v102, v106, v107
	v_cvt_pk_bf16_f32 v103, v108, v109
	s_nop 1
	v_mfma_f32_32x32x16_bf16 v[50:65], v[84:87], v[100:103], v[50:65]
	v_mfma_f32_32x32x16_bf16 v[34:49], v[88:91], v[100:103], v[34:49]
	v_mfma_f32_32x32x16_bf16 v[18:33], v[92:95], v[100:103], v[18:33]
	v_mfma_f32_32x32x16_bf16 v[2:17], v[96:99], v[100:103], v[2:17]
	v_add_u32_e32 v84, v111, v163
	v_add_u32_e32 v112, v159, v162
	ds_read_b64 v[100:101], v84
	ds_read_b128 v[84:87], v112 offset:49152
	ds_read_b128 v[88:91], v112 offset:51200
	ds_read_b128 v[92:95], v112 offset:53248
	ds_read_b128 v[96:99], v112 offset:55296
	s_waitcnt lgkmcnt(0)
	v_cvt_pk_f32_fp8_e32 v[102:103], v100
	v_cvt_pk_f32_fp8_sdwa v[104:105], v100 src0_sel:WORD_1
	v_cvt_pk_f32_fp8_e32 v[106:107], v101
	v_cvt_pk_f32_fp8_sdwa v[108:109], v101 src0_sel:WORD_1
	v_cvt_pk_bf16_f32 v100, v102, v103
	v_cvt_pk_bf16_f32 v101, v104, v105
	v_cvt_pk_bf16_f32 v102, v106, v107
	v_cvt_pk_bf16_f32 v103, v108, v109
	s_nop 0
	v_mfma_f32_32x32x16_bf16 v[50:65], v[84:87], v[100:103], v[50:65]
	v_mfma_f32_32x32x16_bf16 v[34:49], v[88:91], v[100:103], v[34:49]
	v_mfma_f32_32x32x16_bf16 v[18:33], v[92:95], v[100:103], v[18:33]
	v_mfma_f32_32x32x16_bf16 v[2:17], v[96:99], v[100:103], v[2:17]
	s_waitcnt vmcnt(5)
	s_mov_b32 m0, s53
	s_waitcnt lgkmcnt(0)
	s_barrier
	v_lshl_add_u64 v[84:85], v[82:83], 0, s[10:11]
	global_load_lds_dwordx4 v[84:85], off
	s_addk_i32 s52, 0x402
	s_bfe_u32 s10, s52, 0x70009
	s_mul_i32 s10, s10, 3
	s_sub_i32 s10, s36, s10
	s_add_i32 s10, s10, 6
	s_and_b32 s10, s10, 0xff
	s_lshl_b32 s10, s10, 14
	s_add_i32 s36, s39, s10
	s_waitcnt vmcnt(4)
	s_cmp_lt_u32 s37, 12
	v_cvt_pk_bf16_f32 v74, v74, v78
	ds_write_b32 v167, v74 offset:49152
	v_cvt_pk_bf16_f32 v74, v75, v79
	s_cselect_b32 s10, s35, 0x1e0
	ds_write_b32 v167, v74 offset:49216
	v_cvt_pk_bf16_f32 v74, v76, v80
	s_lshl_b64 s[50:51], s[10:11], 13
	ds_write_b32 v167, v74 offset:49280
	v_cvt_pk_bf16_f32 v74, v77, v81
	ds_write_b32 v167, v74 offset:49344
	v_lshl_add_u64 v[78:79], v[154:155], 0, s[50:51]
	global_load_dwordx4 v[74:77], v[78:79], off sc1 nt
	v_lshl_add_u64 v[78:79], v[78:79], 0, s[20:21]
	global_load_dwordx4 v[78:81], v[78:79], off sc1 nt
	v_add_u32_e32 v111, s36, v158
	v_add_u32_e32 v84, v111, v161
	ds_read_b64 v[100:101], v84
	ds_read_b128 v[84:87], v110 offset:57344
	ds_read_b128 v[88:91], v110 offset:59392
	ds_read_b128 v[92:95], v110 offset:61440
	ds_read_b128 v[96:99], v110 offset:63488
	s_waitcnt lgkmcnt(0)
	v_cvt_pk_f32_fp8_e32 v[102:103], v100
	v_cvt_pk_f32_fp8_sdwa v[104:105], v100 src0_sel:WORD_1
	v_cvt_pk_f32_fp8_e32 v[106:107], v101
	v_cvt_pk_f32_fp8_sdwa v[108:109], v101 src0_sel:WORD_1
	v_cvt_pk_bf16_f32 v100, v102, v103
	v_cvt_pk_bf16_f32 v101, v104, v105
	v_cvt_pk_bf16_f32 v102, v106, v107
	v_cvt_pk_bf16_f32 v103, v108, v109
	s_nop 1
	v_mfma_f32_32x32x16_bf16 v[50:65], v[84:87], v[100:103], v[50:65]
	v_mfma_f32_32x32x16_bf16 v[34:49], v[88:91], v[100:103], v[34:49]
	v_mfma_f32_32x32x16_bf16 v[18:33], v[92:95], v[100:103], v[18:33]
	v_mfma_f32_32x32x16_bf16 v[2:17], v[96:99], v[100:103], v[2:17]
	v_add_u32_e32 v84, v111, v163
	ds_read_b64 v[100:101], v84
	ds_read_b128 v[84:87], v112 offset:57344
	ds_read_b128 v[88:91], v112 offset:59392
	ds_read_b128 v[92:95], v112 offset:61440
	ds_read_b128 v[96:99], v112 offset:63488
	s_waitcnt lgkmcnt(0)
	v_cvt_pk_f32_fp8_e32 v[102:103], v100
	v_cvt_pk_f32_fp8_sdwa v[104:105], v100 src0_sel:WORD_1
	v_cvt_pk_f32_fp8_e32 v[106:107], v101
	v_cvt_pk_f32_fp8_sdwa v[108:109], v101 src0_sel:WORD_1
	v_cvt_pk_bf16_f32 v100, v102, v103
	v_cvt_pk_bf16_f32 v101, v104, v105
	v_cvt_pk_bf16_f32 v102, v106, v107
	v_cvt_pk_bf16_f32 v103, v108, v109
	s_nop 0
	v_mfma_f32_32x32x16_bf16 v[50:65], v[84:87], v[100:103], v[50:65]
	v_mfma_f32_32x32x16_bf16 v[34:49], v[88:91], v[100:103], v[34:49]
	v_mfma_f32_32x32x16_bf16 v[18:33], v[92:95], v[100:103], v[18:33]
	v_mfma_f32_32x32x16_bf16 v[2:17], v[96:99], v[100:103], v[2:17]
	s_waitcnt vmcnt(5)
	s_mov_b32 m0, s36
	s_waitcnt lgkmcnt(0)
	s_barrier
	v_lshl_add_u64 v[84:85], v[82:83], 0, s[10:11]
	global_load_lds_dwordx4 v[84:85], off
	s_add_i32 s35, s35, 64
	s_cmp_gt_u32 s37, 13
	s_mov_b32 s36, s37
	s_cbranch_scc0 .Lmoe_B_1087

.LBB0_1089:
	v_mov_b32_e32 v129, 0
	s_and_b64 vcc, exec, s[36:37]
	v_mov_b32_e32 v128, v129
	v_mov_b32_e32 v127, v129
	v_mov_b32_e32 v126, v129
	v_mov_b32_e32 v125, v129
	v_mov_b32_e32 v124, v129
	v_mov_b32_e32 v123, v129
	v_mov_b32_e32 v122, v129
	v_mov_b32_e32 v121, v129
	v_mov_b32_e32 v120, v129
	v_mov_b32_e32 v119, v129
	v_mov_b32_e32 v118, v129
	v_mov_b32_e32 v117, v129
	v_mov_b32_e32 v116, v129
	v_mov_b32_e32 v115, v129
	v_mov_b32_e32 v114, v129
	v_mov_b32_e32 v113, v129
	v_mov_b32_e32 v112, v129
	v_mov_b32_e32 v111, v129
	v_mov_b32_e32 v110, v129
	v_mov_b32_e32 v109, v129
	v_mov_b32_e32 v108, v129
	v_mov_b32_e32 v107, v129
	v_mov_b32_e32 v106, v129
	v_mov_b32_e32 v105, v129
	v_mov_b32_e32 v104, v129
	v_mov_b32_e32 v103, v129
	v_mov_b32_e32 v102, v129
	v_mov_b32_e32 v101, v129
	v_mov_b32_e32 v100, v129
	v_mov_b32_e32 v99, v129
	v_mov_b32_e32 v98, v129
	v_mov_b32_e32 v97, v129
	v_mov_b32_e32 v96, v129
	v_mov_b32_e32 v95, v129
	v_mov_b32_e32 v94, v129
	v_mov_b32_e32 v93, v129
	v_mov_b32_e32 v92, v129
	v_mov_b32_e32 v91, v129
	v_mov_b32_e32 v90, v129
	v_mov_b32_e32 v89, v129
	v_mov_b32_e32 v88, v129
	v_mov_b32_e32 v87, v129
	v_mov_b32_e32 v86, v129
	v_mov_b32_e32 v85, v129
	v_mov_b32_e32 v84, v129
	v_mov_b32_e32 v83, v129
	v_mov_b32_e32 v82, v129
	v_mov_b32_e32 v81, v129
	v_mov_b32_e32 v80, v129
	v_mov_b32_e32 v79, v129
	v_mov_b32_e32 v78, v129
	v_mov_b32_e32 v77, v129
	v_mov_b32_e32 v76, v129
	v_mov_b32_e32 v75, v129
	v_mov_b32_e32 v74, v129
	v_mov_b32_e32 v73, v129
	v_mov_b32_e32 v72, v129
	v_mov_b32_e32 v71, v129
	v_mov_b32_e32 v70, v129
	v_mov_b32_e32 v69, v129
	v_mov_b32_e32 v68, v129
	v_mov_b32_e32 v67, v129
	v_mov_b32_e32 v66, v129
	s_cbranch_vccz .LBB0_1093
	v_cmp_gt_i32_e32 vcc, s48, v165
	s_mov_b32 m0, s39
	v_mov_b32_e32 v157, v147
	v_cndmask_b32_e32 v2, 0, v165, vcc
	v_add_u32_e32 v2, s49, v2
	v_lshl_or_b32 v156, v2, 9, v1
	global_load_dwordx4 v[2:5], v[154:155], off sc1 nt
	global_load_dwordx4 v[6:9], v[132:133], off sc1 nt
	global_load_lds_dwordx4 v146, s[12:13]
	s_mov_b32 m0, s42
	s_nop 0
	global_load_lds_dwordx4 v156, s[12:13]
	global_load_dwordx4 v[130:133], v[130:131], off sc1 nt
	global_load_dwordx4 v[134:137], v[134:135], off sc1 nt
	s_mov_b32 m0, s40
	s_nop 0
	global_load_lds_dwordx4 v146, s[14:15]
	s_mov_b32 m0, s43
	s_nop 0
	global_load_lds_dwordx4 v156, s[14:15]
	s_waitcnt vmcnt(6)
	s_nop 0
	v_cvt_pk_bf16_f32 v2, v2, v6
	ds_write_b32 v167, v2 offset:49152
	v_cvt_pk_bf16_f32 v2, v3, v7
	ds_write_b32 v167, v2 offset:49216
	v_cvt_pk_bf16_f32 v2, v4, v8
	ds_write_b32 v167, v2 offset:49280
	v_cvt_pk_bf16_f32 v2, v5, v9
	ds_write_b32 v167, v2 offset:49344
	global_load_dwordx4 v[138:141], v[138:139], off sc1 nt
	global_load_dwordx4 v[142:145], v[142:143], off sc1 nt
	s_waitcnt vmcnt(6)
	s_mov_b32 m0, s41
	s_waitcnt lgkmcnt(0)
	s_barrier
	global_load_lds_dwordx4 v146, s[16:17]
	s_mov_b32 m0, s44
	v_mov_b32_e32 v66, 0
	global_load_lds_dwordx4 v156, s[16:17]
	s_mov_b32 s36, -2
	s_movk_i32 s35, 0x80
	v_mov_b32_e32 v67, v66
	v_mov_b32_e32 v68, v66
	v_mov_b32_e32 v69, v66
	v_mov_b32_e32 v70, v66
	v_mov_b32_e32 v71, v66
	v_mov_b32_e32 v72, v66
	v_mov_b32_e32 v73, v66
	v_mov_b32_e32 v74, v66
	v_mov_b32_e32 v75, v66
	v_mov_b32_e32 v76, v66
	v_mov_b32_e32 v77, v66
	v_mov_b32_e32 v78, v66
	v_mov_b32_e32 v79, v66
	v_mov_b32_e32 v80, v66
	v_mov_b32_e32 v81, v66
	v_mov_b32_e32 v82, v66
	v_mov_b32_e32 v83, v66
	v_mov_b32_e32 v84, v66
	v_mov_b32_e32 v85, v66
	v_mov_b32_e32 v86, v66
	v_mov_b32_e32 v87, v66
	v_mov_b32_e32 v88, v66
	v_mov_b32_e32 v89, v66
	v_mov_b32_e32 v90, v66
	v_mov_b32_e32 v91, v66
	v_mov_b32_e32 v92, v66
	v_mov_b32_e32 v93, v66
	v_mov_b32_e32 v94, v66
	v_mov_b32_e32 v95, v66
	v_mov_b32_e32 v96, v66
	v_mov_b32_e32 v97, v66
	v_mov_b32_e32 v98, v66
	v_mov_b32_e32 v99, v66
	v_mov_b32_e32 v100, v66
	v_mov_b32_e32 v101, v66
	v_mov_b32_e32 v102, v66
	v_mov_b32_e32 v103, v66
	v_mov_b32_e32 v104, v66
	v_mov_b32_e32 v105, v66
	v_mov_b32_e32 v106, v66
	v_mov_b32_e32 v107, v66
	v_mov_b32_e32 v108, v66
	v_mov_b32_e32 v109, v66
	v_mov_b32_e32 v110, v66
	v_mov_b32_e32 v111, v66
	v_mov_b32_e32 v112, v66
	v_mov_b32_e32 v113, v66
	v_mov_b32_e32 v114, v66
	v_mov_b32_e32 v115, v66
	v_mov_b32_e32 v116, v66
	v_mov_b32_e32 v117, v66
	v_mov_b32_e32 v118, v66
	v_mov_b32_e32 v119, v66
	v_mov_b32_e32 v120, v66
	v_mov_b32_e32 v121, v66
	v_mov_b32_e32 v122, v66
	v_mov_b32_e32 v123, v66
	v_mov_b32_e32 v124, v66
	v_mov_b32_e32 v125, v66
	v_mov_b32_e32 v126, v66
	v_mov_b32_e32 v127, v66
	v_mov_b32_e32 v128, v66
	v_mov_b32_e32 v129, v66
	v_mov_b32_e32 v2, v66
	v_mov_b32_e32 v3, v66
	v_mov_b32_e32 v4, v66
	v_mov_b32_e32 v5, v66
	v_mov_b32_e32 v6, v66
	v_mov_b32_e32 v7, v66
	v_mov_b32_e32 v8, v66
	v_mov_b32_e32 v9, v66
	v_mov_b32_e32 v10, v66
	v_mov_b32_e32 v11, v66
	v_mov_b32_e32 v12, v66
	v_mov_b32_e32 v13, v66
	v_mov_b32_e32 v14, v66
	v_mov_b32_e32 v15, v66
	v_mov_b32_e32 v16, v66
	v_mov_b32_e32 v17, v66
	v_mov_b32_e32 v18, v66
	v_mov_b32_e32 v19, v66
	v_mov_b32_e32 v20, v66
	v_mov_b32_e32 v21, v66
	v_mov_b32_e32 v22, v66
	v_mov_b32_e32 v23, v66
	v_mov_b32_e32 v24, v66
	v_mov_b32_e32 v25, v66
	v_mov_b32_e32 v26, v66
	v_mov_b32_e32 v27, v66
	v_mov_b32_e32 v28, v66
	v_mov_b32_e32 v29, v66
	v_mov_b32_e32 v30, v66
	v_mov_b32_e32 v31, v66
	v_mov_b32_e32 v32, v66
	v_mov_b32_e32 v33, v66
	v_mov_b32_e32 v34, v66
	v_mov_b32_e32 v35, v66
	v_mov_b32_e32 v36, v66
	v_mov_b32_e32 v37, v66
	v_mov_b32_e32 v38, v66
	v_mov_b32_e32 v39, v66
	v_mov_b32_e32 v40, v66
	v_mov_b32_e32 v41, v66
	v_mov_b32_e32 v42, v66
	v_mov_b32_e32 v43, v66
	v_mov_b32_e32 v44, v66
	v_mov_b32_e32 v45, v66
	v_mov_b32_e32 v46, v66
	v_mov_b32_e32 v47, v66
	v_mov_b32_e32 v48, v66
	v_mov_b32_e32 v49, v66
	v_mov_b32_e32 v50, v66
	v_mov_b32_e32 v51, v66
	v_mov_b32_e32 v52, v66
	v_mov_b32_e32 v53, v66
	v_mov_b32_e32 v54, v66
	v_mov_b32_e32 v55, v66
	v_mov_b32_e32 v56, v66
	v_mov_b32_e32 v57, v66
	v_mov_b32_e32 v58, v66
	v_mov_b32_e32 v59, v66
	v_mov_b32_e32 v60, v66
	v_mov_b32_e32 v61, v66
	v_mov_b32_e32 v62, v66
	v_mov_b32_e32 v63, v66
	v_mov_b32_e32 v64, v66
	v_mov_b32_e32 v65, v66
	v_readfirstlane_b32 s98, v250
	s_bitcmp1_b32 s98, 8
	s_cbranch_scc1 .Lmoe_B_1091
.LBB0_1091:
	s_mul_i32 s49, s36, 0xab
	s_add_i32 s10, s49, 0x357
	s_bfe_u32 s10, s10, 0x70009
	s_mul_i32 s10, s10, 3
	s_sub_i32 s10, s36, s10
	s_add_i32 s10, s10, 5
	s_and_b32 s10, s10, 0xff
	s_lshl_b32 s10, s10, 14
	s_add_i32 s50, s39, s10
	s_add_i32 s37, s36, 2
	v_add_u32_e32 v200, s50, v158
	v_add_u32_e32 v196, v200, v161
	v_add_u32_e32 v169, v159, v160
	ds_read_b64 v[186:187], v196
	ds_read_b128 v[170:173], v169 offset:49152
	ds_read_b128 v[174:177], v169 offset:51200
	ds_read_b128 v[178:181], v169 offset:53248
	ds_read_b128 v[182:185], v169 offset:55296
	s_waitcnt lgkmcnt(0)
	v_cvt_pk_f32_fp8_e32 v[188:189], v186
	v_cvt_pk_f32_fp8_sdwa v[190:191], v186 src0_sel:WORD_1
	v_cvt_pk_f32_fp8_e32 v[192:193], v187
	v_cvt_pk_f32_fp8_sdwa v[194:195], v187 src0_sel:WORD_1
	v_cvt_pk_bf16_f32 v186, v188, v189
	v_cvt_pk_bf16_f32 v187, v190, v191
	v_cvt_pk_bf16_f32 v188, v192, v193
	v_cvt_pk_bf16_f32 v189, v194, v195
	ds_read_b64 v[190:191], v196 offset:8192
	s_waitcnt lgkmcnt(0)
	v_cvt_pk_f32_fp8_e32 v[192:193], v190
	v_cvt_pk_f32_fp8_sdwa v[194:195], v190 src0_sel:WORD_1
	v_cvt_pk_f32_fp8_e32 v[196:197], v191
	v_cvt_pk_f32_fp8_sdwa v[198:199], v191 src0_sel:WORD_1
	v_cvt_pk_bf16_f32 v190, v192, v193
	v_cvt_pk_bf16_f32 v191, v194, v195
	v_cvt_pk_bf16_f32 v192, v196, v197
	v_cvt_pk_bf16_f32 v193, v198, v199
	s_waitcnt vmcnt(6)
	s_sub_i32 s10, s35, 32
	v_cvt_pk_bf16_f32 v130, v130, v134
	s_cmp_lt_u32 s37, 13
	ds_write_b32 v167, v130 offset:57344
	v_cvt_pk_bf16_f32 v130, v131, v135
	s_cselect_b32 s10, s10, 0x1e0
	ds_write_b32 v167, v130 offset:57408
	v_cvt_pk_bf16_f32 v130, v132, v136
	s_lshl_b64 s[52:53], s[10:11], 13
	ds_write_b32 v167, v130 offset:57472
	v_cvt_pk_bf16_f32 v130, v133, v137
	ds_write_b32 v167, v130 offset:57536
	v_lshl_add_u64 v[134:135], v[154:155], 0, s[52:53]
	global_load_dwordx4 v[130:133], v[134:135], off sc1 nt
	v_lshl_add_u64 v[134:135], v[134:135], 0, s[20:21]
	global_load_dwordx4 v[134:137], v[134:135], off sc1 nt
	v_mfma_f32_32x32x16_bf16 v[50:65], v[170:173], v[186:189], v[50:65]
	v_mfma_f32_32x32x16_bf16 v[34:49], v[174:177], v[186:189], v[34:49]
	v_mfma_f32_32x32x16_bf16 v[18:33], v[178:181], v[186:189], v[18:33]
	v_mfma_f32_32x32x16_bf16 v[2:17], v[182:185], v[186:189], v[2:17]
	v_mfma_f32_32x32x16_bf16 v[114:129], v[170:173], v[190:193], v[114:129]
	v_mfma_f32_32x32x16_bf16 v[98:113], v[174:177], v[190:193], v[98:113]
	v_mfma_f32_32x32x16_bf16 v[82:97], v[178:181], v[190:193], v[82:97]
	v_mfma_f32_32x32x16_bf16 v[66:81], v[182:185], v[190:193], v[66:81]
	v_add_u32_e32 v196, v200, v163
	v_add_u32_e32 v201, v159, v162
	ds_read_b64 v[186:187], v196
	ds_read_b128 v[170:173], v201 offset:49152
	ds_read_b128 v[174:177], v201 offset:51200
	ds_read_b128 v[178:181], v201 offset:53248
	ds_read_b128 v[182:185], v201 offset:55296
	s_waitcnt lgkmcnt(0)
	v_cvt_pk_f32_fp8_e32 v[188:189], v186
	v_cvt_pk_f32_fp8_sdwa v[190:191], v186 src0_sel:WORD_1
	v_cvt_pk_f32_fp8_e32 v[192:193], v187
	v_cvt_pk_f32_fp8_sdwa v[194:195], v187 src0_sel:WORD_1
	v_cvt_pk_bf16_f32 v186, v188, v189
	v_cvt_pk_bf16_f32 v187, v190, v191
	v_cvt_pk_bf16_f32 v188, v192, v193
	v_cvt_pk_bf16_f32 v189, v194, v195
	ds_read_b64 v[190:191], v196 offset:8192
	v_mfma_f32_32x32x16_bf16 v[50:65], v[170:173], v[186:189], v[50:65]
	s_waitcnt lgkmcnt(0)
	v_cvt_pk_f32_fp8_e32 v[192:193], v190
	v_cvt_pk_f32_fp8_e32 v[194:195], v191
	v_mfma_f32_32x32x16_bf16 v[34:49], v[174:177], v[186:189], v[34:49]
	v_mfma_f32_32x32x16_bf16 v[18:33], v[178:181], v[186:189], v[18:33]
	v_mfma_f32_32x32x16_bf16 v[2:17], v[182:185], v[186:189], v[2:17]
	v_cvt_pk_f32_fp8_sdwa v[188:189], v190 src0_sel:WORD_1
	v_cvt_pk_f32_fp8_sdwa v[190:191], v191 src0_sel:WORD_1
	v_cvt_pk_bf16_f32 v186, v192, v193
	v_cvt_pk_bf16_f32 v187, v188, v189
	v_cvt_pk_bf16_f32 v188, v194, v195
	v_cvt_pk_bf16_f32 v189, v190, v191
	s_nop 0
	v_mfma_f32_32x32x16_bf16 v[114:129], v[170:173], v[186:189], v[114:129]
	v_mfma_f32_32x32x16_bf16 v[98:113], v[174:177], v[186:189], v[98:113]
	v_mfma_f32_32x32x16_bf16 v[82:97], v[178:181], v[186:189], v[82:97]
	v_mfma_f32_32x32x16_bf16 v[66:81], v[182:185], v[186:189], v[66:81]
	s_add_u32 s52, s12, s10
	s_waitcnt vmcnt(6)
	s_addc_u32 s53, s13, 0
	s_mov_b32 m0, s50
	s_waitcnt lgkmcnt(0)
	s_barrier
	v_lshl_add_u64 v[170:171], s[52:53], 0, v[146:147]
	global_load_lds_dwordx4 v[170:171], off
	v_lshl_add_u64 v[170:171], s[52:53], 0, v[156:157]
	s_add_i32 m0, s50, 0x2000
	s_addk_i32 s49, 0x402
	global_load_lds_dwordx4 v[170:171], off
	s_bfe_u32 s10, s49, 0x70009
	s_mul_i32 s10, s10, 3
	s_sub_i32 s10, s36, s10
	s_add_i32 s10, s10, 6
	s_and_b32 s10, s10, 0xff
	s_lshl_b32 s10, s10, 14
	s_add_i32 s36, s39, s10
	v_add_u32_e32 v200, s36, v158
	v_add_u32_e32 v196, v200, v161
	ds_read_b64 v[186:187], v196
	ds_read_b128 v[170:173], v169 offset:57344
	ds_read_b128 v[174:177], v169 offset:59392
	ds_read_b128 v[178:181], v169 offset:61440
	ds_read_b128 v[182:185], v169 offset:63488
	s_waitcnt lgkmcnt(0)
	v_cvt_pk_f32_fp8_e32 v[188:189], v186
	v_cvt_pk_f32_fp8_sdwa v[190:191], v186 src0_sel:WORD_1
	v_cvt_pk_f32_fp8_e32 v[192:193], v187
	v_cvt_pk_f32_fp8_sdwa v[194:195], v187 src0_sel:WORD_1
	v_cvt_pk_bf16_f32 v186, v188, v189
	v_cvt_pk_bf16_f32 v187, v190, v191
	v_cvt_pk_bf16_f32 v188, v192, v193
	v_cvt_pk_bf16_f32 v189, v194, v195
	ds_read_b64 v[190:191], v196 offset:8192
	s_waitcnt lgkmcnt(0)
	v_cvt_pk_f32_fp8_e32 v[192:193], v190
	v_cvt_pk_f32_fp8_sdwa v[194:195], v190 src0_sel:WORD_1
	v_cvt_pk_f32_fp8_e32 v[196:197], v191
	v_cvt_pk_f32_fp8_sdwa v[198:199], v191 src0_sel:WORD_1
	v_cvt_pk_bf16_f32 v190, v192, v193
	v_cvt_pk_bf16_f32 v191, v194, v195
	v_cvt_pk_bf16_f32 v192, v196, v197
	v_cvt_pk_bf16_f32 v193, v198, v199
	s_waitcnt vmcnt(6)
	s_cmp_lt_u32 s37, 12
	v_cvt_pk_bf16_f32 v138, v138, v142
	ds_write_b32 v167, v138 offset:49152
	v_cvt_pk_bf16_f32 v138, v139, v143
	s_cselect_b32 s10, s35, 0x1e0
	ds_write_b32 v167, v138 offset:49216
	v_cvt_pk_bf16_f32 v138, v140, v144
	s_lshl_b64 s[50:51], s[10:11], 13
	ds_write_b32 v167, v138 offset:49280
	v_cvt_pk_bf16_f32 v138, v141, v145
	ds_write_b32 v167, v138 offset:49344
	v_lshl_add_u64 v[142:143], v[154:155], 0, s[50:51]
	global_load_dwordx4 v[138:141], v[142:143], off sc1 nt
	v_lshl_add_u64 v[142:143], v[142:143], 0, s[20:21]
	global_load_dwordx4 v[142:145], v[142:143], off sc1 nt
	v_mfma_f32_32x32x16_bf16 v[50:65], v[170:173], v[186:189], v[50:65]
	v_mfma_f32_32x32x16_bf16 v[34:49], v[174:177], v[186:189], v[34:49]
	v_mfma_f32_32x32x16_bf16 v[18:33], v[178:181], v[186:189], v[18:33]
	v_mfma_f32_32x32x16_bf16 v[2:17], v[182:185], v[186:189], v[2:17]
	v_mfma_f32_32x32x16_bf16 v[114:129], v[170:173], v[190:193], v[114:129]
	v_mfma_f32_32x32x16_bf16 v[98:113], v[174:177], v[190:193], v[98:113]
	v_mfma_f32_32x32x16_bf16 v[82:97], v[178:181], v[190:193], v[82:97]
	v_mfma_f32_32x32x16_bf16 v[66:81], v[182:185], v[190:193], v[66:81]
	v_add_u32_e32 v169, v200, v163
	ds_read_b64 v[186:187], v169
	ds_read_b128 v[170:173], v201 offset:57344
	ds_read_b128 v[174:177], v201 offset:59392
	ds_read_b128 v[178:181], v201 offset:61440
	ds_read_b128 v[182:185], v201 offset:63488
	s_waitcnt lgkmcnt(0)
	v_cvt_pk_f32_fp8_e32 v[188:189], v186
	v_cvt_pk_f32_fp8_sdwa v[190:191], v186 src0_sel:WORD_1
	v_cvt_pk_f32_fp8_e32 v[192:193], v187
	v_cvt_pk_f32_fp8_sdwa v[194:195], v187 src0_sel:WORD_1
	v_cvt_pk_bf16_f32 v186, v188, v189
	v_cvt_pk_bf16_f32 v187, v190, v191
	v_cvt_pk_bf16_f32 v188, v192, v193
	v_cvt_pk_bf16_f32 v189, v194, v195
	ds_read_b64 v[190:191], v169 offset:8192
	v_mfma_f32_32x32x16_bf16 v[50:65], v[170:173], v[186:189], v[50:65]
	s_waitcnt lgkmcnt(0)
	v_cvt_pk_f32_fp8_e32 v[192:193], v190
	v_cvt_pk_f32_fp8_e32 v[194:195], v191
	v_mfma_f32_32x32x16_bf16 v[34:49], v[174:177], v[186:189], v[34:49]
	v_mfma_f32_32x32x16_bf16 v[18:33], v[178:181], v[186:189], v[18:33]
	v_mfma_f32_32x32x16_bf16 v[2:17], v[182:185], v[186:189], v[2:17]
	v_cvt_pk_f32_fp8_sdwa v[188:189], v190 src0_sel:WORD_1
	v_cvt_pk_f32_fp8_sdwa v[190:191], v191 src0_sel:WORD_1
	v_cvt_pk_bf16_f32 v186, v192, v193
	v_cvt_pk_bf16_f32 v187, v188, v189
	v_cvt_pk_bf16_f32 v188, v194, v195
	v_cvt_pk_bf16_f32 v189, v190, v191
	s_nop 0
	v_mfma_f32_32x32x16_bf16 v[114:129], v[170:173], v[186:189], v[114:129]
	v_mfma_f32_32x32x16_bf16 v[98:113], v[174:177], v[186:189], v[98:113]
	v_mfma_f32_32x32x16_bf16 v[82:97], v[178:181], v[186:189], v[82:97]
	v_mfma_f32_32x32x16_bf16 v[66:81], v[182:185], v[186:189], v[66:81]
	s_add_u32 s50, s12, s10
	s_waitcnt vmcnt(6)
	s_addc_u32 s51, s13, 0
	s_mov_b32 m0, s36
	s_waitcnt lgkmcnt(0)
	s_barrier
	v_lshl_add_u64 v[170:171], s[50:51], 0, v[146:147]
	global_load_lds_dwordx4 v[170:171], off
	v_lshl_add_u64 v[170:171], s[50:51], 0, v[156:157]
	s_add_i32 m0, s36, 0x2000
	s_add_i32 s35, s35, 64
	global_load_lds_dwordx4 v[170:171], off
	s_cmp_gt_u32 s37, 13
	s_mov_b32 s36, s37
	s_cbranch_scc0 .LBB0_1091
	s_branch .Lmoe_X_1091
.Lmoe_B_1091:
	s_mul_i32 s49, s36, 0xab
	s_add_i32 s10, s49, 0x357
	s_bfe_u32 s10, s10, 0x70009
	s_mul_i32 s10, s10, 3
	s_sub_i32 s10, s36, s10
	s_add_i32 s10, s10, 5
	s_and_b32 s10, s10, 0xff
	s_lshl_b32 s10, s10, 14
	s_add_i32 s50, s39, s10
	s_add_i32 s37, s36, 2
	s_waitcnt vmcnt(6)
	s_sub_i32 s10, s35, 32
	v_cvt_pk_bf16_f32 v130, v130, v134
	s_cmp_lt_u32 s37, 13
	ds_write_b32 v167, v130 offset:57344
	v_cvt_pk_bf16_f32 v130, v131, v135
	s_cselect_b32 s10, s10, 0x1e0
	ds_write_b32 v167, v130 offset:57408
	v_cvt_pk_bf16_f32 v130, v132, v136
	s_lshl_b64 s[52:53], s[10:11], 13
	ds_write_b32 v167, v130 offset:57472
	v_cvt_pk_bf16_f32 v130, v133, v137
	ds_write_b32 v167, v130 offset:57536
	v_lshl_add_u64 v[134:135], v[154:155], 0, s[52:53]
	global_load_dwordx4 v[130:133], v[134:135], off sc1 nt
	v_lshl_add_u64 v[134:135], v[134:135], 0, s[20:21]
	global_load_dwordx4 v[134:137], v[134:135], off sc1 nt
	v_add_u32_e32 v200, s50, v158
	v_add_u32_e32 v196, v200, v161
	v_add_u32_e32 v169, v159, v160
	ds_read_b64 v[186:187], v196
	ds_read_b128 v[170:173], v169 offset:49152
	ds_read_b128 v[174:177], v169 offset:51200
	ds_read_b128 v[178:181], v169 offset:53248
	ds_read_b128 v[182:185], v169 offset:55296
	s_waitcnt lgkmcnt(0)
	v_cvt_pk_f32_fp8_e32 v[188:189], v186
	v_cvt_pk_f32_fp8_sdwa v[190:191], v186 src0_sel:WORD_1
	v_cvt_pk_f32_fp8_e32 v[192:193], v187
	v_cvt_pk_f32_fp8_sdwa v[194:195], v187 src0_sel:WORD_1
	v_cvt_pk_bf16_f32 v186, v188, v189
	v_cvt_pk_bf16_f32 v187, v190, v191
	v_cvt_pk_bf16_f32 v188, v192, v193
	v_cvt_pk_bf16_f32 v189, v194, v195
	ds_read_b64 v[190:191], v196 offset:8192
	s_waitcnt lgkmcnt(0)
	v_cvt_pk_f32_fp8_e32 v[192:193], v190
	v_cvt_pk_f32_fp8_sdwa v[194:195], v190 src0_sel:WORD_1
	v_cvt_pk_f32_fp8_e32 v[196:197], v191
	v_cvt_pk_f32_fp8_sdwa v[198:199], v191 src0_sel:WORD_1
	v_cvt_pk_bf16_f32 v190, v192, v193
	v_cvt_pk_bf16_f32 v191, v194, v195
	v_cvt_pk_bf16_f32 v192, v196, v197
	v_cvt_pk_bf16_f32 v193, v198, v199
	s_nop 1
	v_mfma_f32_32x32x16_bf16 v[50:65], v[170:173], v[186:189], v[50:65]
	v_mfma_f32_32x32x16_bf16 v[34:49], v[174:177], v[186:189], v[34:49]
	v_mfma_f32_32x32x16_bf16 v[18:33], v[178:181], v[186:189], v[18:33]
	v_mfma_f32_32x32x16_bf16 v[2:17], v[182:185], v[186:189], v[2:17]
	v_mfma_f32_32x32x16_bf16 v[114:129], v[170:173], v[190:193], v[114:129]
	v_mfma_f32_32x32x16_bf16 v[98:113], v[174:177], v[190:193], v[98:113]
	v_mfma_f32_32x32x16_bf16 v[82:97], v[178:181], v[190:193], v[82:97]
	v_mfma_f32_32x32x16_bf16 v[66:81], v[182:185], v[190:193], v[66:81]
	v_add_u32_e32 v196, v200, v163
	v_add_u32_e32 v201, v159, v162
	ds_read_b64 v[186:187], v196
	ds_read_b128 v[170:173], v201 offset:49152
	ds_read_b128 v[174:177], v201 offset:51200
	ds_read_b128 v[178:181], v201 offset:53248
	ds_read_b128 v[182:185], v201 offset:55296
	s_waitcnt lgkmcnt(0)
	v_cvt_pk_f32_fp8_e32 v[188:189], v186
	v_cvt_pk_f32_fp8_sdwa v[190:191], v186 src0_sel:WORD_1
	v_cvt_pk_f32_fp8_e32 v[192:193], v187
	v_cvt_pk_f32_fp8_sdwa v[194:195], v187 src0_sel:WORD_1
	v_cvt_pk_bf16_f32 v186, v188, v189
	v_cvt_pk_bf16_f32 v187, v190, v191
	v_cvt_pk_bf16_f32 v188, v192, v193
	v_cvt_pk_bf16_f32 v189, v194, v195
	ds_read_b64 v[190:191], v196 offset:8192
	v_mfma_f32_32x32x16_bf16 v[50:65], v[170:173], v[186:189], v[50:65]
	s_waitcnt lgkmcnt(0)
	v_cvt_pk_f32_fp8_e32 v[192:193], v190
	v_cvt_pk_f32_fp8_e32 v[194:195], v191
	v_mfma_f32_32x32x16_bf16 v[34:49], v[174:177], v[186:189], v[34:49]
	v_mfma_f32_32x32x16_bf16 v[18:33], v[178:181], v[186:189], v[18:33]
	v_mfma_f32_32x32x16_bf16 v[2:17], v[182:185], v[186:189], v[2:17]
	v_cvt_pk_f32_fp8_sdwa v[188:189], v190 src0_sel:WORD_1
	v_cvt_pk_f32_fp8_sdwa v[190:191], v191 src0_sel:WORD_1
	v_cvt_pk_bf16_f32 v186, v192, v193
	v_cvt_pk_bf16_f32 v187, v188, v189
	v_cvt_pk_bf16_f32 v188, v194, v195
	v_cvt_pk_bf16_f32 v189, v190, v191
	s_nop 0
	v_mfma_f32_32x32x16_bf16 v[114:129], v[170:173], v[186:189], v[114:129]
	v_mfma_f32_32x32x16_bf16 v[98:113], v[174:177], v[186:189], v[98:113]
	v_mfma_f32_32x32x16_bf16 v[82:97], v[178:181], v[186:189], v[82:97]
	v_mfma_f32_32x32x16_bf16 v[66:81], v[182:185], v[186:189], v[66:81]
	s_add_u32 s52, s12, s10
	s_waitcnt vmcnt(6)
	s_addc_u32 s53, s13, 0
	s_mov_b32 m0, s50
	s_waitcnt lgkmcnt(0)
	s_barrier
	v_lshl_add_u64 v[170:171], s[52:53], 0, v[146:147]
	global_load_lds_dwordx4 v[170:171], off
	v_lshl_add_u64 v[170:171], s[52:53], 0, v[156:157]
	s_add_i32 m0, s50, 0x2000
	s_addk_i32 s49, 0x402
	global_load_lds_dwordx4 v[170:171], off
	s_bfe_u32 s10, s49, 0x70009
	s_mul_i32 s10, s10, 3
	s_sub_i32 s10, s36, s10
	s_add_i32 s10, s10, 6
	s_and_b32 s10, s10, 0xff
	s_lshl_b32 s10, s10, 14
	s_add_i32 s36, s39, s10
	s_waitcnt vmcnt(6)
	s_cmp_lt_u32 s37, 12
	v_cvt_pk_bf16_f32 v138, v138, v142
	ds_write_b32 v167, v138 offset:49152
	v_cvt_pk_bf16_f32 v138, v139, v143
	s_cselect_b32 s10, s35, 0x1e0
	ds_write_b32 v167, v138 offset:49216
	v_cvt_pk_bf16_f32 v138, v140, v144
	s_lshl_b64 s[50:51], s[10:11], 13
	ds_write_b32 v167, v138 offset:49280
	v_cvt_pk_bf16_f32 v138, v141, v145
	ds_write_b32 v167, v138 offset:49344
	v_lshl_add_u64 v[142:143], v[154:155], 0, s[50:51]
	global_load_dwordx4 v[138:141], v[142:143], off sc1 nt
	v_lshl_add_u64 v[142:143], v[142:143], 0, s[20:21]
	global_load_dwordx4 v[142:145], v[142:143], off sc1 nt
	v_add_u32_e32 v200, s36, v158
	v_add_u32_e32 v196, v200, v161
	ds_read_b64 v[186:187], v196
	ds_read_b128 v[170:173], v169 offset:57344
	ds_read_b128 v[174:177], v169 offset:59392
	ds_read_b128 v[178:181], v169 offset:61440
	ds_read_b128 v[182:185], v169 offset:63488
	s_waitcnt lgkmcnt(0)
	v_cvt_pk_f32_fp8_e32 v[188:189], v186
	v_cvt_pk_f32_fp8_sdwa v[190:191], v186 src0_sel:WORD_1
	v_cvt_pk_f32_fp8_e32 v[192:193], v187
	v_cvt_pk_f32_fp8_sdwa v[194:195], v187 src0_sel:WORD_1
	v_cvt_pk_bf16_f32 v186, v188, v189
	v_cvt_pk_bf16_f32 v187, v190, v191
	v_cvt_pk_bf16_f32 v188, v192, v193
	v_cvt_pk_bf16_f32 v189, v194, v195
	ds_read_b64 v[190:191], v196 offset:8192
	s_waitcnt lgkmcnt(0)
	v_cvt_pk_f32_fp8_e32 v[192:193], v190
	v_cvt_pk_f32_fp8_sdwa v[194:195], v190 src0_sel:WORD_1
	v_cvt_pk_f32_fp8_e32 v[196:197], v191
	v_cvt_pk_f32_fp8_sdwa v[198:199], v191 src0_sel:WORD_1
	v_cvt_pk_bf16_f32 v190, v192, v193
	v_cvt_pk_bf16_f32 v191, v194, v195
	v_cvt_pk_bf16_f32 v192, v196, v197
	v_cvt_pk_bf16_f32 v193, v198, v199
	s_nop 1
	v_mfma_f32_32x32x16_bf16 v[50:65], v[170:173], v[186:189], v[50:65]
	v_mfma_f32_32x32x16_bf16 v[34:49], v[174:177], v[186:189], v[34:49]
	v_mfma_f32_32x32x16_bf16 v[18:33], v[178:181], v[186:189], v[18:33]
	v_mfma_f32_32x32x16_bf16 v[2:17], v[182:185], v[186:189], v[2:17]
	v_mfma_f32_32x32x16_bf16 v[114:129], v[170:173], v[190:193], v[114:129]
	v_mfma_f32_32x32x16_bf16 v[98:113], v[174:177], v[190:193], v[98:113]
	v_mfma_f32_32x32x16_bf16 v[82:97], v[178:181], v[190:193], v[82:97]
	v_mfma_f32_32x32x16_bf16 v[66:81], v[182:185], v[190:193], v[66:81]
	v_add_u32_e32 v169, v200, v163
	ds_read_b64 v[186:187], v169
	ds_read_b128 v[170:173], v201 offset:57344
	ds_read_b128 v[174:177], v201 offset:59392
	ds_read_b128 v[178:181], v201 offset:61440
	ds_read_b128 v[182:185], v201 offset:63488
	s_waitcnt lgkmcnt(0)
	v_cvt_pk_f32_fp8_e32 v[188:189], v186
	v_cvt_pk_f32_fp8_sdwa v[190:191], v186 src0_sel:WORD_1
	v_cvt_pk_f32_fp8_e32 v[192:193], v187
	v_cvt_pk_f32_fp8_sdwa v[194:195], v187 src0_sel:WORD_1
	v_cvt_pk_bf16_f32 v186, v188, v189
	v_cvt_pk_bf16_f32 v187, v190, v191
	v_cvt_pk_bf16_f32 v188, v192, v193
	v_cvt_pk_bf16_f32 v189, v194, v195
	ds_read_b64 v[190:191], v169 offset:8192
	v_mfma_f32_32x32x16_bf16 v[50:65], v[170:173], v[186:189], v[50:65]
	s_waitcnt lgkmcnt(0)
	v_cvt_pk_f32_fp8_e32 v[192:193], v190
	v_cvt_pk_f32_fp8_e32 v[194:195], v191
	v_mfma_f32_32x32x16_bf16 v[34:49], v[174:177], v[186:189], v[34:49]
	v_mfma_f32_32x32x16_bf16 v[18:33], v[178:181], v[186:189], v[18:33]
	v_mfma_f32_32x32x16_bf16 v[2:17], v[182:185], v[186:189], v[2:17]
	v_cvt_pk_f32_fp8_sdwa v[188:189], v190 src0_sel:WORD_1
	v_cvt_pk_f32_fp8_sdwa v[190:191], v191 src0_sel:WORD_1
	v_cvt_pk_bf16_f32 v186, v192, v193
	v_cvt_pk_bf16_f32 v187, v188, v189
	v_cvt_pk_bf16_f32 v188, v194, v195
	v_cvt_pk_bf16_f32 v189, v190, v191
	s_nop 0
	v_mfma_f32_32x32x16_bf16 v[114:129], v[170:173], v[186:189], v[114:129]
	v_mfma_f32_32x32x16_bf16 v[98:113], v[174:177], v[186:189], v[98:113]
	v_mfma_f32_32x32x16_bf16 v[82:97], v[178:181], v[186:189], v[82:97]
	v_mfma_f32_32x32x16_bf16 v[66:81], v[182:185], v[186:189], v[66:81]
	s_add_u32 s50, s12, s10
	s_waitcnt vmcnt(6)
	s_addc_u32 s51, s13, 0
	s_mov_b32 m0, s36
	s_waitcnt lgkmcnt(0)
	s_barrier
	v_lshl_add_u64 v[170:171], s[50:51], 0, v[146:147]
	global_load_lds_dwordx4 v[170:171], off
	v_lshl_add_u64 v[170:171], s[50:51], 0, v[156:157]
	s_add_i32 m0, s36, 0x2000
	s_add_i32 s35, s35, 64
	global_load_lds_dwordx4 v[170:171], off
	s_cmp_gt_u32 s37, 13
	s_mov_b32 s36, s37
	s_cbranch_scc0 .Lmoe_B_1091
.Lmoe_X_1091:
	s_waitcnt vmcnt(0)
.LBB0_1093:
	s_waitcnt vmcnt(0)
	s_lshl_b32 s10, s34, 13
	s_mulk_i32 s34, 0x44
	s_add_i32 s36, s34, 0
	s_add_i32 s36, s36, 0x20400
	v_cmp_gt_i32_e32 vcc, s48, v164
	s_and_saveexec_b64 s[34:35], vcc
	s_cbranch_execz .LBB0_1095
	v_mov_b32_e32 v130, s36
	ds_read_b32 v130, v130 offset:32
	v_add_u32_e32 v131, s47, v164
	v_med3_f32 v134, v51, s45, v168
	v_med3_f32 v135, v53, s45, v168
	v_add_u32_e32 v53, s10, v131
	s_waitcnt lgkmcnt(0)
	v_cmp_gt_i32_e32 vcc, v130, v131
	v_med3_f32 v139, v18, s45, v168
	v_med3_f32 v140, v19, s45, v168
	v_cndmask_b32_e64 v130, 8, 0, vcc
	v_lshl_add_u32 v132, v130, 2, s36
	ds_read_b32 v132, v132 offset:16
	v_or_b32_e32 v133, 4, v130
	v_mov_b32_e32 v18, v147
	v_cvt_pk_fp8_f32 v18, v139, v140
	v_med3_f32 v20, v20, s45, v168
	s_waitcnt lgkmcnt(0)
	v_cmp_gt_i32_e32 vcc, v132, v131
	v_med3_f32 v21, v21, s45, v168
	v_cvt_pk_fp8_f32 v18, v20, v21 op_sel:[0,0,1]
	v_cndmask_b32_e32 v130, v133, v130, vcc
	v_lshl_add_u32 v132, v130, 2, s36
	ds_read_b32 v132, v132 offset:8
	v_med3_f32 v133, v50, s45, v168
	v_or_b32_e32 v50, 2, v130
	v_med3_f32 v22, v22, s45, v168
	v_med3_f32 v23, v23, s45, v168
	s_waitcnt lgkmcnt(0)
	v_cmp_gt_i32_e32 vcc, v132, v131
	v_med3_f32 v132, v52, s45, v168
	v_mov_b32_e32 v19, v147
	v_cndmask_b32_e32 v51, v50, v130, vcc
	v_lshl_add_u32 v50, v51, 2, s36
	ds_read_b32 v130, v50 offset:4
	v_or_b32_e32 v52, 1, v51
	v_cvt_pk_fp8_f32 v19, v22, v23
	v_med3_f32 v26, v26, s45, v168
	v_mov_b32_e32 v50, v147
	s_waitcnt lgkmcnt(0)
	v_cmp_gt_i32_e32 vcc, v130, v131
	v_med3_f32 v54, v54, s45, v168
	v_med3_f32 v55, v55, s45, v168
	v_cndmask_b32_e32 v51, v52, v51, vcc
	v_lshl_add_u32 v52, v51, 2, s36
	ds_read_b32 v52, v52
	v_med3_f32 v58, v58, s45, v168
	v_med3_f32 v59, v59, s45, v168
	v_med3_f32 v62, v62, s45, v168
	v_med3_f32 v63, v63, s45, v168
	s_waitcnt lgkmcnt(0)
	v_sub_u32_e32 v52, v53, v52
	v_lshl_add_u32 v52, v51, 9, v52
	v_ashrrev_i32_e32 v53, 31, v52
	v_lshl_add_u64 v[52:53], v[52:53], 2, s[8:9]
	global_load_dword v130, v[52:53], off
	v_mov_b32_e32 v51, v147
	v_mov_b32_e32 v52, v147
	v_mov_b32_e32 v53, v147
	v_med3_f32 v131, v34, s45, v168
	v_med3_f32 v136, v35, s45, v168
	v_med3_f32 v137, v36, s45, v168
	v_med3_f32 v138, v37, s45, v168
	v_mov_b32_e32 v34, v147
	v_med3_f32 v38, v38, s45, v168
	v_med3_f32 v39, v39, s45, v168
	v_mov_b32_e32 v35, v147
	v_med3_f32 v42, v42, s45, v168
	v_med3_f32 v43, v43, s45, v168
	v_mov_b32_e32 v36, v147
	v_med3_f32 v46, v46, s45, v168
	v_med3_f32 v47, v47, s45, v168
	v_mov_b32_e32 v37, v147
	v_cvt_pk_fp8_f32 v50, v133, v134
	v_cvt_pk_fp8_f32 v51, v54, v55
	v_cvt_pk_fp8_f32 v52, v58, v59
	v_cvt_pk_fp8_f32 v53, v62, v63
	v_med3_f32 v24, v24, s45, v168
	v_med3_f32 v25, v25, s45, v168
	v_cvt_pk_fp8_f32 v34, v131, v136
	v_cvt_pk_fp8_f32 v35, v38, v39
	v_cvt_pk_fp8_f32 v36, v42, v43
	v_cvt_pk_fp8_f32 v37, v46, v47
	v_cvt_pk_fp8_f32 v19, v24, v25 op_sel:[0,0,1]
	v_med3_f32 v24, v28, s45, v168
	v_med3_f32 v25, v29, s45, v168
	v_med3_f32 v56, v56, s45, v168
	v_med3_f32 v57, v57, s45, v168
	v_med3_f32 v60, v60, s45, v168
	v_med3_f32 v61, v61, s45, v168
	v_med3_f32 v64, v64, s45, v168
	v_med3_f32 v65, v65, s45, v168
	v_med3_f32 v40, v40, s45, v168
	v_med3_f32 v41, v41, s45, v168
	v_med3_f32 v44, v44, s45, v168
	v_med3_f32 v45, v45, s45, v168
	v_med3_f32 v48, v48, s45, v168
	v_med3_f32 v49, v49, s45, v168
	v_cvt_pk_fp8_f32 v50, v132, v135 op_sel:[0,0,1]
	v_cvt_pk_fp8_f32 v51, v56, v57 op_sel:[0,0,1]
	v_cvt_pk_fp8_f32 v52, v60, v61 op_sel:[0,0,1]
	v_cvt_pk_fp8_f32 v53, v64, v65 op_sel:[0,0,1]
	v_cvt_pk_fp8_f32 v34, v137, v138 op_sel:[0,0,1]
	v_cvt_pk_fp8_f32 v35, v40, v41 op_sel:[0,0,1]
	v_cvt_pk_fp8_f32 v36, v44, v45 op_sel:[0,0,1]
	v_cvt_pk_fp8_f32 v37, v48, v49 op_sel:[0,0,1]
	v_permlane32_swap_b32_e32 v50, v51
	v_permlane32_swap_b32_e32 v52, v53
	v_permlane32_swap_b32_e32 v18, v19
	v_permlane32_swap_b32_e32 v34, v35
	v_permlane32_swap_b32_e32 v36, v37
	v_permlane32_swap_b32_e32 v50, v52
	v_permlane32_swap_b32_e32 v51, v53
	v_permlane32_swap_b32_e32 v34, v36
	v_permlane32_swap_b32_e32 v35, v37
	v_med3_f32 v3, v3, s45, v168
	v_med3_f32 v6, v6, s45, v168
	v_med3_f32 v7, v7, s45, v168
	v_med3_f32 v4, v4, s45, v168
	v_med3_f32 v5, v5, s45, v168
	s_waitcnt vmcnt(0)
	v_ashrrev_i32_e32 v20, 16, v130
	v_ashrrev_i32_e32 v21, 31, v20
	v_lshlrev_b32_e32 v22, 11, v130
	v_lshlrev_b64 v[20:21], 24, v[20:21]
	v_and_b32_e32 v146, 0x7fff800, v22
	v_lshl_add_u64 v[20:21], s[18:19], 0, v[20:21]
	v_lshl_add_u64 v[20:21], v[20:21], 0, v[146:147]
	v_lshl_add_u64 v[20:21], v[20:21], 0, s[30:31]
	v_lshl_add_u64 v[22:23], v[20:21], 0, v[150:151]
	v_med3_f32 v21, v27, s45, v168
	v_mov_b32_e32 v20, v147
	v_cvt_pk_fp8_f32 v20, v26, v21
	v_med3_f32 v26, v30, s45, v168
	v_med3_f32 v27, v31, s45, v168
	v_mov_b32_e32 v21, v147
	v_cvt_pk_fp8_f32 v21, v26, v27
	v_cvt_pk_fp8_f32 v20, v24, v25 op_sel:[0,0,1]
	v_med3_f32 v24, v32, s45, v168
	v_med3_f32 v25, v33, s45, v168
	v_cvt_pk_fp8_f32 v21, v24, v25 op_sel:[0,0,1]
	global_store_dwordx4 v[22:23], v[50:53], off
	global_store_dwordx4 v[22:23], v[34:37], off offset:32
	v_permlane32_swap_b32_e32 v20, v21
	s_nop 1
	v_permlane32_swap_b32_e32 v18, v20
	v_permlane32_swap_b32_e32 v19, v21
	global_store_dwordx4 v[22:23], v[18:21], off offset:64
	s_nop 1
	v_med3_f32 v18, v2, s45, v168
	v_mov_b32_e32 v2, v147
	v_cvt_pk_fp8_f32 v2, v18, v3
	v_mov_b32_e32 v3, v147
	v_cvt_pk_fp8_f32 v3, v6, v7
	v_med3_f32 v6, v11, s45, v168
	v_cvt_pk_fp8_f32 v2, v4, v5 op_sel:[0,0,1]
	v_med3_f32 v4, v8, s45, v168
	v_med3_f32 v5, v9, s45, v168
	v_cvt_pk_fp8_f32 v3, v4, v5 op_sel:[0,0,1]
	v_med3_f32 v5, v10, s45, v168
	v_mov_b32_e32 v4, v147
	v_cvt_pk_fp8_f32 v4, v5, v6
	v_med3_f32 v6, v14, s45, v168
	v_med3_f32 v9, v15, s45, v168
	v_mov_b32_e32 v5, v147
	v_cvt_pk_fp8_f32 v5, v6, v9
	v_med3_f32 v7, v12, s45, v168
	v_med3_f32 v8, v13, s45, v168
	v_cvt_pk_fp8_f32 v4, v7, v8 op_sel:[0,0,1]
	v_med3_f32 v6, v16, s45, v168
	v_med3_f32 v7, v17, s45, v168
	v_cvt_pk_fp8_f32 v5, v6, v7 op_sel:[0,0,1]
	v_permlane32_swap_b32_e32 v2, v3
	s_nop 0
	v_permlane32_swap_b32_e32 v4, v5
	s_nop 1
	v_permlane32_swap_b32_e32 v2, v4
	v_permlane32_swap_b32_e32 v3, v5
	global_store_dwordx4 v[22:23], v[2:5], off offset:96
